# v35 + attention VALU trims: QK C-init replication via v_mov_b64 (8 instead of 15 movs), row-sum accumulators start from the first exp pair (no x+0 init)
# baseline (speedup 1.0000x reference)
.LBB0_833:
	s_add_i32 s30, s72, -1
	s_cmp_ge_u32 s30, s90
	s_cbranch_scc1 .LBB0_846
	s_cmp_lt_u32 s72, s90
	v_cmp_eq_f32_e64 s[30:31], s1, v173
	s_cselect_b64 s[52:53], -1, 0
	s_cmp_ge_u32 s72, s90
	v_cndmask_b32_e64 v185, v173, 0, s[30:31]
	s_cbranch_scc1 .LBB0_836
	s_mul_i32 s34, s71, 0x6000
	v_add_u32_e32 v147, s34, v169
	ds_read_b128 v[148:151], v147
	v_xor_b32_e32 v98, 0x80000000, v185
	v_mov_b32_e32 v99, v98
	v_mov_b64_e32 v[100:101], v[98:99]
	v_mov_b64_e32 v[102:103], v[98:99]
	v_mov_b64_e32 v[104:105], v[98:99]
	v_mov_b64_e32 v[106:107], v[98:99]
	v_mov_b64_e32 v[108:109], v[98:99]
	v_mov_b64_e32 v[110:111], v[98:99]
	v_mov_b64_e32 v[112:113], v[98:99]
	ds_read_b128 v[152:155], v147 offset:4096
	v_add_u32_e32 v147, s34, v170
	ds_read_b128 v[156:159], v147
	ds_read_b128 v[188:191], v147 offset:4096
	v_add_u32_e32 v147, s34, v171
	ds_read_b128 v[192:195], v147
	ds_read_b128 v[196:199], v147 offset:4096
	v_add_u32_e32 v147, s34, v172
	ds_read_b128 v[208:211], v147
	ds_read_b128 v[212:215], v147 offset:4096
	s_waitcnt lgkmcnt(7)
	s_nop 0
	v_mfma_f32_32x32x16_f16 v[114:129], v[148:151], v[130:133], v[98:113]
	s_waitcnt lgkmcnt(6)
	v_mfma_f32_32x32x16_f16 v[98:113], v[152:155], v[130:133], v[98:113]
	s_waitcnt lgkmcnt(5)
	v_mfma_f32_32x32x16_f16 v[114:129], v[156:159], v[134:137], v[114:129]
	s_waitcnt lgkmcnt(4)
	v_mfma_f32_32x32x16_f16 v[98:113], v[188:191], v[134:137], v[98:113]
	s_waitcnt lgkmcnt(3)
	v_mfma_f32_32x32x16_f16 v[114:129], v[192:195], v[138:141], v[114:129]
	s_waitcnt lgkmcnt(2)
	v_mfma_f32_32x32x16_f16 v[98:113], v[196:199], v[138:141], v[98:113]
	s_waitcnt lgkmcnt(1)
	v_mfma_f32_32x32x16_f16 v[114:129], v[208:211], v[142:145], v[114:129]
	s_waitcnt lgkmcnt(0)
	v_mfma_f32_32x32x16_f16 v[98:113], v[212:215], v[142:145], v[98:113]

.LBB0_842:
	v_exp_f32_e32 v2, v2
	v_exp_f32_e32 v3, v3
	v_exp_f32_e32 v4, v4
	v_exp_f32_e32 v5, v5
	v_exp_f32_e32 v6, v6
	v_exp_f32_e32 v7, v7
	v_exp_f32_e32 v18, v18
	v_exp_f32_e32 v19, v19
	v_exp_f32_e32 v8, v8
	v_exp_f32_e32 v9, v9
	v_exp_f32_e32 v20, v20
	v_exp_f32_e32 v21, v21
	v_exp_f32_e32 v10, v10
	v_exp_f32_e32 v11, v11
	v_pk_add_f32 v[208:209], v[4:5], v[2:3]
	v_exp_f32_e32 v22, v22
	v_exp_f32_e32 v23, v23
	v_exp_f32_e32 v24, v24
	v_exp_f32_e32 v25, v25
	v_exp_f32_e32 v12, v12
	v_exp_f32_e32 v13, v13
	v_pk_add_f32 v[208:209], v[6:7], v[208:209]
	v_pk_add_f32 v[208:209], v[8:9], v[208:209]
	v_exp_f32_e32 v26, v26
	v_exp_f32_e32 v27, v27
	v_pk_add_f32 v[196:197], v[20:21], v[18:19]
	v_exp_f32_e32 v28, v28
	v_exp_f32_e32 v29, v29
	v_pk_add_f32 v[208:209], v[10:11], v[208:209]
	v_pk_add_f32 v[196:197], v[22:23], v[196:197]
	v_pk_add_f32 v[212:213], v[12:13], v[208:209]
	v_exp_f32_e32 v30, v30
	v_exp_f32_e32 v31, v31
	v_exp_f32_e32 v14, v14
	v_exp_f32_e32 v15, v15
	v_cvt_pk_f16_f32 v208, v18, v19
	v_cvt_pk_f16_f32 v209, v20, v21
	v_cvt_pk_f16_f32 v210, v22, v23
	v_cvt_pk_f16_f32 v211, v24, v25
	v_pk_add_f32 v[196:197], v[24:25], v[196:197]
	v_exp_f32_e32 v32, v32
	v_exp_f32_e32 v33, v33
	s_waitcnt lgkmcnt(0)
	v_mfma_f32_32x32x16_f16 v[82:97], v[158:161], v[208:211], v[82:97]
	v_exp_f32_e32 v16, v16
	v_exp_f32_e32 v17, v17
	v_pk_add_f32 v[196:197], v[26:27], v[196:197]
	v_pk_add_f32 v[160:161], v[14:15], v[212:213]
	v_pk_add_f32 v[196:197], v[28:29], v[196:197]
	v_pk_add_f32 v[160:161], v[16:17], v[160:161]
	v_pk_add_f32 v[158:159], v[30:31], v[196:197]
	v_mfma_f32_32x32x16_f16 v[66:81], v[154:157], v[208:211], v[66:81]
	v_add_f32_e64 v158, v32, v158
	v_add_f32_e64 v159, v33, v159
	v_cvt_pk_f16_f32 v154, v26, v27
	v_add_f32_e64 v158, v160, v158
	v_add_f32_e64 v159, v161, v159
	v_cvt_pk_f16_f32 v155, v28, v29
	v_add_f32_e32 v195, v158, v159
	v_add_f32_e32 v184, v184, v195
	v_cvt_pk_f16_f32 v156, v30, v31
	v_mfma_f32_32x32x16_f16 v[50:65], v[150:153], v[208:211], v[50:65]
	v_cvt_pk_f16_f32 v157, v32, v33
	v_cvt_pk_f16_f32 v158, v2, v3
	v_cvt_pk_f16_f32 v159, v4, v5
	v_cvt_pk_f16_f32 v160, v6, v7
	v_cvt_pk_f16_f32 v161, v8, v9
	v_cvt_pk_f16_f32 v150, v10, v11
	v_cvt_pk_f16_f32 v151, v12, v13
	v_mfma_f32_32x32x16_f16 v[34:49], v[146:149], v[208:211], v[34:49]
	v_cvt_pk_f16_f32 v152, v14, v15
	v_cvt_pk_f16_f32 v153, v16, v17
	s_and_b64 vcc, exec, s[34:35]
	ds_read_b64_tr_b16 v[146:147], v192 offset:12288
	ds_read_b64_tr_b16 v[148:149], v193 offset:12288
	ds_read_b64_tr_b16 v[196:197], v191 offset:12288
	ds_read_b64_tr_b16 v[198:199], v186 offset:12288
	ds_read_b64_tr_b16 v[212:213], v189 offset:12288
	ds_read_b64_tr_b16 v[214:215], v187 offset:12288
	ds_read_b64_tr_b16 v[216:217], v190 offset:12288
	ds_read_b64_tr_b16 v[218:219], v188 offset:12288
	ds_read_b64_tr_b16 v[220:221], v192 offset:16384
	ds_read_b64_tr_b16 v[222:223], v193 offset:16384
	s_waitcnt lgkmcnt(8)
	v_mfma_f32_32x32x16_f16 v[82:97], v[146:149], v[154:157], v[82:97]
	ds_read_b64_tr_b16 v[224:225], v191 offset:16384
	ds_read_b64_tr_b16 v[226:227], v186 offset:16384
	s_waitcnt lgkmcnt(8)
	v_mfma_f32_32x32x16_f16 v[66:81], v[196:199], v[154:157], v[66:81]
	ds_read_b64_tr_b16 v[146:147], v189 offset:16384
	ds_read_b64_tr_b16 v[148:149], v187 offset:16384
	s_waitcnt lgkmcnt(8)
	v_mfma_f32_32x32x16_f16 v[50:65], v[212:215], v[154:157], v[50:65]
	ds_read_b64_tr_b16 v[196:197], v190 offset:16384
	ds_read_b64_tr_b16 v[198:199], v188 offset:16384
	s_waitcnt lgkmcnt(8)
	v_mfma_f32_32x32x16_f16 v[34:49], v[216:219], v[154:157], v[34:49]
	ds_read_b64_tr_b16 v[212:213], v192 offset:20480
	ds_read_b64_tr_b16 v[214:215], v193 offset:20480
	s_waitcnt lgkmcnt(8)
	v_mfma_f32_32x32x16_f16 v[82:97], v[220:223], v[158:161], v[82:97]
	ds_read_b64_tr_b16 v[216:217], v191 offset:20480
	ds_read_b64_tr_b16 v[218:219], v186 offset:20480
	s_waitcnt lgkmcnt(8)
	v_mfma_f32_32x32x16_f16 v[66:81], v[224:227], v[158:161], v[66:81]
	ds_read_b64_tr_b16 v[220:221], v189 offset:20480
	ds_read_b64_tr_b16 v[222:223], v187 offset:20480
	s_waitcnt lgkmcnt(8)
	v_mfma_f32_32x32x16_f16 v[50:65], v[146:149], v[158:161], v[50:65]
	ds_read_b64_tr_b16 v[224:225], v190 offset:20480
	ds_read_b64_tr_b16 v[226:227], v188 offset:20480
	s_waitcnt lgkmcnt(8)
	v_mfma_f32_32x32x16_f16 v[34:49], v[196:199], v[158:161], v[34:49]
	s_waitcnt lgkmcnt(6)
	v_mfma_f32_32x32x16_f16 v[82:97], v[212:215], v[150:153], v[82:97]
	s_waitcnt lgkmcnt(4)
	v_mfma_f32_32x32x16_f16 v[66:81], v[216:219], v[150:153], v[66:81]
	s_waitcnt lgkmcnt(2)
	v_mfma_f32_32x32x16_f16 v[50:65], v[220:223], v[150:153], v[50:65]
	s_waitcnt lgkmcnt(0)
	v_mfma_f32_32x32x16_f16 v[34:49], v[224:227], v[150:153], v[34:49]
	v_mov_b32_e32 v146, 0
	s_cbranch_vccnz .LBB0_846
	s_mov_b32 s29, 0x41000000
	v_cmp_lg_f32_e64 s[34:35], s1, v194
	v_cmp_lt_f32_e32 vcc, s29, v194
	s_and_b64 s[30:31], s[30:31], s[34:35]
	s_or_b64 s[30:31], vcc, s[30:31]
	v_cndmask_b32_e64 v146, 0, 1, s[30:31]
	v_cmp_ne_u32_e32 vcc, 0, v146
	s_cbranch_vccz .LBB0_845
	v_add_f32_e32 v146, v185, v194
	v_max_f32_e32 v147, v173, v173
	v_max_f32_e32 v173, v147, v146
	v_cmp_neq_f32_e32 vcc, s1, v173
	s_nop 1
	v_cndmask_b32_e32 v146, 0, v173, vcc
	v_sub_f32_e32 v146, v146, v185
	v_exp_f32_e64 v148, -v146
	s_nop 0
	v_pk_mul_f32 v[96:97], v[148:149], v[96:97] op_sel_hi:[0,1]
	v_pk_mul_f32 v[94:95], v[148:149], v[94:95] op_sel_hi:[0,1]
	v_pk_mul_f32 v[92:93], v[148:149], v[92:93] op_sel_hi:[0,1]
	v_pk_mul_f32 v[90:91], v[148:149], v[90:91] op_sel_hi:[0,1]
	v_pk_mul_f32 v[88:89], v[148:149], v[88:89] op_sel_hi:[0,1]
	v_pk_mul_f32 v[86:87], v[148:149], v[86:87] op_sel_hi:[0,1]
	v_pk_mul_f32 v[84:85], v[148:149], v[84:85] op_sel_hi:[0,1]
	v_pk_mul_f32 v[82:83], v[148:149], v[82:83] op_sel_hi:[0,1]
	v_pk_mul_f32 v[80:81], v[148:149], v[80:81] op_sel_hi:[0,1]
	v_pk_mul_f32 v[78:79], v[148:149], v[78:79] op_sel_hi:[0,1]
	v_pk_mul_f32 v[76:77], v[148:149], v[76:77] op_sel_hi:[0,1]
	v_pk_mul_f32 v[74:75], v[148:149], v[74:75] op_sel_hi:[0,1]
	v_pk_mul_f32 v[72:73], v[148:149], v[72:73] op_sel_hi:[0,1]
	v_pk_mul_f32 v[70:71], v[148:149], v[70:71] op_sel_hi:[0,1]
	v_pk_mul_f32 v[68:69], v[148:149], v[68:69] op_sel_hi:[0,1]
	v_pk_mul_f32 v[66:67], v[148:149], v[66:67] op_sel_hi:[0,1]
	v_pk_mul_f32 v[64:65], v[148:149], v[64:65] op_sel_hi:[0,1]
	v_pk_mul_f32 v[62:63], v[148:149], v[62:63] op_sel_hi:[0,1]
	v_pk_mul_f32 v[60:61], v[148:149], v[60:61] op_sel_hi:[0,1]
	v_pk_mul_f32 v[58:59], v[148:149], v[58:59] op_sel_hi:[0,1]
	v_pk_mul_f32 v[56:57], v[148:149], v[56:57] op_sel_hi:[0,1]
	v_pk_mul_f32 v[54:55], v[148:149], v[54:55] op_sel_hi:[0,1]
	v_pk_mul_f32 v[52:53], v[148:149], v[52:53] op_sel_hi:[0,1]
	v_pk_mul_f32 v[50:51], v[148:149], v[50:51] op_sel_hi:[0,1]
	v_pk_mul_f32 v[48:49], v[148:149], v[48:49] op_sel_hi:[0,1]
	v_pk_mul_f32 v[46:47], v[148:149], v[46:47] op_sel_hi:[0,1]
	v_pk_mul_f32 v[44:45], v[148:149], v[44:45] op_sel_hi:[0,1]
	v_pk_mul_f32 v[42:43], v[148:149], v[42:43] op_sel_hi:[0,1]
	v_pk_mul_f32 v[40:41], v[148:149], v[40:41] op_sel_hi:[0,1]
	v_pk_mul_f32 v[38:39], v[148:149], v[38:39] op_sel_hi:[0,1]
	v_pk_mul_f32 v[36:37], v[148:149], v[36:37] op_sel_hi:[0,1]
	v_pk_mul_f32 v[34:35], v[148:149], v[34:35] op_sel_hi:[0,1]
	v_mul_f32_e32 v184, v184, v148
	s_branch .LBB0_846

.LBB0_851:
	s_cmp_ge_u32 s72, s90
	s_cbranch_scc1 .LBB0_865
	s_cmp_lt_u32 s74, s90
	v_cmp_eq_f32_e64 s[30:31], s1, v173
	s_cselect_b64 s[52:53], -1, 0
	s_cmp_ge_u32 s74, s90
	v_cndmask_b32_e64 v185, v173, 0, s[30:31]
	s_cbranch_scc1 .LBB0_854
	s_mul_i32 s34, s75, 0x6000
	v_add_u32_e32 v147, s34, v169
	ds_read_b128 v[148:151], v147
	v_xor_b32_e32 v2, 0x80000000, v185
	v_mov_b32_e32 v3, v2
	v_mov_b64_e32 v[4:5], v[2:3]
	v_mov_b64_e32 v[6:7], v[2:3]
	v_mov_b64_e32 v[8:9], v[2:3]
	v_mov_b64_e32 v[10:11], v[2:3]
	v_mov_b64_e32 v[12:13], v[2:3]
	v_mov_b64_e32 v[14:15], v[2:3]
	v_mov_b64_e32 v[16:17], v[2:3]
	ds_read_b128 v[152:155], v147 offset:4096
	v_add_u32_e32 v147, s34, v170
	ds_read_b128 v[156:159], v147
	ds_read_b128 v[188:191], v147 offset:4096
	v_add_u32_e32 v147, s34, v171
	ds_read_b128 v[192:195], v147
	ds_read_b128 v[196:199], v147 offset:4096
	v_add_u32_e32 v147, s34, v172
	ds_read_b128 v[208:211], v147
	ds_read_b128 v[212:215], v147 offset:4096
	s_waitcnt lgkmcnt(7)
	s_nop 0
	v_mfma_f32_32x32x16_f16 v[18:33], v[148:151], v[130:133], v[2:17]
	s_waitcnt lgkmcnt(6)
	v_mfma_f32_32x32x16_f16 v[2:17], v[152:155], v[130:133], v[2:17]
	s_waitcnt lgkmcnt(5)
	v_mfma_f32_32x32x16_f16 v[18:33], v[156:159], v[134:137], v[18:33]
	s_waitcnt lgkmcnt(4)
	v_mfma_f32_32x32x16_f16 v[2:17], v[188:191], v[134:137], v[2:17]
	s_waitcnt lgkmcnt(3)
	v_mfma_f32_32x32x16_f16 v[18:33], v[192:195], v[138:141], v[18:33]
	s_waitcnt lgkmcnt(2)
	v_mfma_f32_32x32x16_f16 v[2:17], v[196:199], v[138:141], v[2:17]
	s_waitcnt lgkmcnt(1)
	v_mfma_f32_32x32x16_f16 v[18:33], v[208:211], v[142:145], v[18:33]
	s_waitcnt lgkmcnt(0)
	v_mfma_f32_32x32x16_f16 v[2:17], v[212:215], v[142:145], v[2:17]

.LBB0_860:
	v_exp_f32_e32 v98, v98
	v_exp_f32_e32 v99, v99
	v_exp_f32_e32 v100, v100
	v_exp_f32_e32 v101, v101
	v_exp_f32_e32 v102, v102
	v_exp_f32_e32 v103, v103
	v_exp_f32_e32 v114, v114
	v_exp_f32_e32 v115, v115
	v_exp_f32_e32 v104, v104
	v_exp_f32_e32 v105, v105
	v_exp_f32_e32 v116, v116
	v_exp_f32_e32 v117, v117
	v_exp_f32_e32 v106, v106
	v_exp_f32_e32 v107, v107
	v_pk_add_f32 v[208:209], v[100:101], v[98:99]
	v_exp_f32_e32 v118, v118
	v_exp_f32_e32 v119, v119
	v_exp_f32_e32 v120, v120
	v_exp_f32_e32 v121, v121
	v_exp_f32_e32 v108, v108
	v_exp_f32_e32 v109, v109
	v_pk_add_f32 v[208:209], v[102:103], v[208:209]
	v_pk_add_f32 v[208:209], v[104:105], v[208:209]
	v_exp_f32_e32 v122, v122
	v_exp_f32_e32 v123, v123
	v_pk_add_f32 v[196:197], v[116:117], v[114:115]
	v_exp_f32_e32 v124, v124
	v_exp_f32_e32 v125, v125
	v_pk_add_f32 v[208:209], v[106:107], v[208:209]
	v_pk_add_f32 v[196:197], v[118:119], v[196:197]
	v_pk_add_f32 v[212:213], v[108:109], v[208:209]
	v_exp_f32_e32 v126, v126
	v_exp_f32_e32 v127, v127
	v_exp_f32_e32 v110, v110
	v_exp_f32_e32 v111, v111
	v_cvt_pk_f16_f32 v208, v114, v115
	v_cvt_pk_f16_f32 v209, v116, v117
	v_cvt_pk_f16_f32 v210, v118, v119
	v_cvt_pk_f16_f32 v211, v120, v121
	v_pk_add_f32 v[196:197], v[120:121], v[196:197]
	v_exp_f32_e32 v128, v128
	v_exp_f32_e32 v129, v129
	s_waitcnt lgkmcnt(0)
	v_mfma_f32_32x32x16_f16 v[82:97], v[158:161], v[208:211], v[82:97]
	v_exp_f32_e32 v112, v112
	v_exp_f32_e32 v113, v113
	v_pk_add_f32 v[196:197], v[122:123], v[196:197]
	v_pk_add_f32 v[160:161], v[110:111], v[212:213]
	v_pk_add_f32 v[196:197], v[124:125], v[196:197]
	v_pk_add_f32 v[160:161], v[112:113], v[160:161]
	v_pk_add_f32 v[158:159], v[126:127], v[196:197]
	v_mfma_f32_32x32x16_f16 v[66:81], v[154:157], v[208:211], v[66:81]
	v_add_f32_e64 v158, v128, v158
	v_add_f32_e64 v159, v129, v159
	v_cvt_pk_f16_f32 v154, v122, v123
	v_add_f32_e64 v158, v158, v160
	v_add_f32_e64 v159, v159, v161
	v_cvt_pk_f16_f32 v155, v124, v125
	v_add_f32_e32 v195, v158, v159
	v_add_f32_e32 v184, v184, v195
	v_cvt_pk_f16_f32 v156, v126, v127
	v_mfma_f32_32x32x16_f16 v[50:65], v[150:153], v[208:211], v[50:65]
	v_cvt_pk_f16_f32 v157, v128, v129
	v_cvt_pk_f16_f32 v158, v98, v99
	v_cvt_pk_f16_f32 v159, v100, v101
	v_cvt_pk_f16_f32 v160, v102, v103
	v_cvt_pk_f16_f32 v161, v104, v105
	v_cvt_pk_f16_f32 v150, v106, v107
	v_cvt_pk_f16_f32 v151, v108, v109
	v_mfma_f32_32x32x16_f16 v[34:49], v[146:149], v[208:211], v[34:49]
	v_cvt_pk_f16_f32 v152, v110, v111
	v_cvt_pk_f16_f32 v153, v112, v113
	s_and_b64 vcc, exec, s[34:35]
	ds_read_b64_tr_b16 v[146:147], v192 offset:12288
	ds_read_b64_tr_b16 v[148:149], v193 offset:12288
	ds_read_b64_tr_b16 v[196:197], v191 offset:12288
	ds_read_b64_tr_b16 v[198:199], v186 offset:12288
	ds_read_b64_tr_b16 v[212:213], v189 offset:12288
	ds_read_b64_tr_b16 v[214:215], v187 offset:12288
	ds_read_b64_tr_b16 v[216:217], v190 offset:12288
	ds_read_b64_tr_b16 v[218:219], v188 offset:12288
	ds_read_b64_tr_b16 v[220:221], v192 offset:16384
	ds_read_b64_tr_b16 v[222:223], v193 offset:16384
	s_waitcnt lgkmcnt(8)
	v_mfma_f32_32x32x16_f16 v[82:97], v[146:149], v[154:157], v[82:97]
	ds_read_b64_tr_b16 v[224:225], v191 offset:16384
	ds_read_b64_tr_b16 v[226:227], v186 offset:16384
	s_waitcnt lgkmcnt(8)
	v_mfma_f32_32x32x16_f16 v[66:81], v[196:199], v[154:157], v[66:81]
	ds_read_b64_tr_b16 v[146:147], v189 offset:16384
	ds_read_b64_tr_b16 v[148:149], v187 offset:16384
	s_waitcnt lgkmcnt(8)
	v_mfma_f32_32x32x16_f16 v[50:65], v[212:215], v[154:157], v[50:65]
	ds_read_b64_tr_b16 v[196:197], v190 offset:16384
	ds_read_b64_tr_b16 v[198:199], v188 offset:16384
	s_waitcnt lgkmcnt(8)
	v_mfma_f32_32x32x16_f16 v[34:49], v[216:219], v[154:157], v[34:49]
	ds_read_b64_tr_b16 v[212:213], v192 offset:20480
	ds_read_b64_tr_b16 v[214:215], v193 offset:20480
	s_waitcnt lgkmcnt(8)
	v_mfma_f32_32x32x16_f16 v[82:97], v[220:223], v[158:161], v[82:97]
	ds_read_b64_tr_b16 v[216:217], v191 offset:20480
	ds_read_b64_tr_b16 v[218:219], v186 offset:20480
	s_waitcnt lgkmcnt(8)
	v_mfma_f32_32x32x16_f16 v[66:81], v[224:227], v[158:161], v[66:81]
	ds_read_b64_tr_b16 v[220:221], v189 offset:20480
	ds_read_b64_tr_b16 v[222:223], v187 offset:20480
	s_waitcnt lgkmcnt(8)
	v_mfma_f32_32x32x16_f16 v[50:65], v[146:149], v[158:161], v[50:65]
	ds_read_b64_tr_b16 v[224:225], v190 offset:20480
	ds_read_b64_tr_b16 v[226:227], v188 offset:20480
	s_waitcnt lgkmcnt(8)
	v_mfma_f32_32x32x16_f16 v[34:49], v[196:199], v[158:161], v[34:49]
	s_waitcnt lgkmcnt(6)
	v_mfma_f32_32x32x16_f16 v[82:97], v[212:215], v[150:153], v[82:97]
	s_waitcnt lgkmcnt(4)
	v_mfma_f32_32x32x16_f16 v[66:81], v[216:219], v[150:153], v[66:81]
	s_waitcnt lgkmcnt(2)
	v_mfma_f32_32x32x16_f16 v[50:65], v[220:223], v[150:153], v[50:65]
	s_waitcnt lgkmcnt(0)
	v_mfma_f32_32x32x16_f16 v[34:49], v[224:227], v[150:153], v[34:49]
	v_mov_b32_e32 v146, 0
	s_cbranch_vccnz .LBB0_865
	s_mov_b32 s29, 0x41000000
	v_cmp_lg_f32_e64 s[34:35], s1, v194
	v_cmp_lt_f32_e32 vcc, s29, v194
	s_and_b64 s[30:31], s[30:31], s[34:35]
	s_or_b64 s[30:31], vcc, s[30:31]
	v_cndmask_b32_e64 v146, 0, 1, s[30:31]
	v_cmp_ne_u32_e32 vcc, 0, v146
	s_cbranch_vccz .LBB0_864
	v_add_f32_e32 v146, v185, v194
	v_max_f32_e32 v147, v173, v173
	v_max_f32_e32 v173, v147, v146
	v_cmp_neq_f32_e32 vcc, s1, v173
	s_nop 1
	v_cndmask_b32_e32 v146, 0, v173, vcc
	v_sub_f32_e32 v146, v146, v185
	v_exp_f32_e64 v148, -v146
	s_nop 0
	v_pk_mul_f32 v[96:97], v[148:149], v[96:97] op_sel_hi:[0,1]
	v_pk_mul_f32 v[94:95], v[148:149], v[94:95] op_sel_hi:[0,1]
	v_pk_mul_f32 v[92:93], v[148:149], v[92:93] op_sel_hi:[0,1]
	v_pk_mul_f32 v[90:91], v[148:149], v[90:91] op_sel_hi:[0,1]
	v_pk_mul_f32 v[88:89], v[148:149], v[88:89] op_sel_hi:[0,1]
	v_pk_mul_f32 v[86:87], v[148:149], v[86:87] op_sel_hi:[0,1]
	v_pk_mul_f32 v[84:85], v[148:149], v[84:85] op_sel_hi:[0,1]
	v_pk_mul_f32 v[82:83], v[148:149], v[82:83] op_sel_hi:[0,1]
	v_pk_mul_f32 v[80:81], v[148:149], v[80:81] op_sel_hi:[0,1]
	v_pk_mul_f32 v[78:79], v[148:149], v[78:79] op_sel_hi:[0,1]
	v_pk_mul_f32 v[76:77], v[148:149], v[76:77] op_sel_hi:[0,1]
	v_pk_mul_f32 v[74:75], v[148:149], v[74:75] op_sel_hi:[0,1]
	v_pk_mul_f32 v[72:73], v[148:149], v[72:73] op_sel_hi:[0,1]
	v_pk_mul_f32 v[70:71], v[148:149], v[70:71] op_sel_hi:[0,1]
	v_pk_mul_f32 v[68:69], v[148:149], v[68:69] op_sel_hi:[0,1]
	v_pk_mul_f32 v[66:67], v[148:149], v[66:67] op_sel_hi:[0,1]
	v_pk_mul_f32 v[64:65], v[148:149], v[64:65] op_sel_hi:[0,1]
	v_pk_mul_f32 v[62:63], v[148:149], v[62:63] op_sel_hi:[0,1]
	v_pk_mul_f32 v[60:61], v[148:149], v[60:61] op_sel_hi:[0,1]
	v_pk_mul_f32 v[58:59], v[148:149], v[58:59] op_sel_hi:[0,1]
	v_pk_mul_f32 v[56:57], v[148:149], v[56:57] op_sel_hi:[0,1]
	v_pk_mul_f32 v[54:55], v[148:149], v[54:55] op_sel_hi:[0,1]
	v_pk_mul_f32 v[52:53], v[148:149], v[52:53] op_sel_hi:[0,1]
	v_pk_mul_f32 v[50:51], v[148:149], v[50:51] op_sel_hi:[0,1]
	v_pk_mul_f32 v[48:49], v[148:149], v[48:49] op_sel_hi:[0,1]
	v_pk_mul_f32 v[46:47], v[148:149], v[46:47] op_sel_hi:[0,1]
	v_pk_mul_f32 v[44:45], v[148:149], v[44:45] op_sel_hi:[0,1]
	v_pk_mul_f32 v[42:43], v[148:149], v[42:43] op_sel_hi:[0,1]
	v_pk_mul_f32 v[40:41], v[148:149], v[40:41] op_sel_hi:[0,1]
	v_pk_mul_f32 v[38:39], v[148:149], v[38:39] op_sel_hi:[0,1]
	v_pk_mul_f32 v[36:37], v[148:149], v[36:37] op_sel_hi:[0,1]
	v_pk_mul_f32 v[34:35], v[148:149], v[34:35] op_sel_hi:[0,1]
	v_mul_f32_e32 v184, v184, v148
	s_branch .LBB0_865

.LBB0_878:
	s_add_i32 s30, s42, -1
	s_cmp_ge_u32 s30, s90
	s_cbranch_scc1 .LBB0_891
	s_cmp_lt_u32 s42, s90
	v_cmp_eq_f32_e64 s[30:31], s1, v172
	s_cselect_b64 s[40:41], -1, 0
	s_cmp_ge_u32 s42, s90
	v_cndmask_b32_e64 v184, v172, 0, s[30:31]
	s_cbranch_scc1 .LBB0_881
	s_mul_i32 s35, s26, 0x6000
	v_add_u32_e32 v147, s35, v168
	ds_read_b128 v[148:151], v147
	v_xor_b32_e32 v98, 0x80000000, v184
	v_mov_b32_e32 v99, v98
	v_mov_b64_e32 v[100:101], v[98:99]
	v_mov_b64_e32 v[102:103], v[98:99]
	v_mov_b64_e32 v[104:105], v[98:99]
	v_mov_b64_e32 v[106:107], v[98:99]
	v_mov_b64_e32 v[108:109], v[98:99]
	v_mov_b64_e32 v[110:111], v[98:99]
	v_mov_b64_e32 v[112:113], v[98:99]
	ds_read_b128 v[152:155], v147 offset:4096
	v_add_u32_e32 v147, s35, v169
	ds_read_b128 v[156:159], v147
	ds_read_b128 v[188:191], v147 offset:4096
	v_add_u32_e32 v147, s35, v170
	ds_read_b128 v[192:195], v147
	ds_read_b128 v[196:199], v147 offset:4096
	v_add_u32_e32 v147, s35, v171
	ds_read_b128 v[208:211], v147
	ds_read_b128 v[212:215], v147 offset:4096
	s_waitcnt lgkmcnt(7)
	s_nop 0
	v_mfma_f32_32x32x16_f16 v[114:129], v[148:151], v[130:133], v[98:113]
	s_waitcnt lgkmcnt(6)
	v_mfma_f32_32x32x16_f16 v[98:113], v[152:155], v[130:133], v[98:113]
	s_waitcnt lgkmcnt(5)
	v_mfma_f32_32x32x16_f16 v[114:129], v[156:159], v[134:137], v[114:129]
	s_waitcnt lgkmcnt(4)
	v_mfma_f32_32x32x16_f16 v[98:113], v[188:191], v[134:137], v[98:113]
	s_waitcnt lgkmcnt(3)
	v_mfma_f32_32x32x16_f16 v[114:129], v[192:195], v[138:141], v[114:129]
	s_waitcnt lgkmcnt(2)
	v_mfma_f32_32x32x16_f16 v[98:113], v[196:199], v[138:141], v[98:113]
	s_waitcnt lgkmcnt(1)
	v_mfma_f32_32x32x16_f16 v[114:129], v[208:211], v[142:145], v[114:129]
	s_waitcnt lgkmcnt(0)
	v_mfma_f32_32x32x16_f16 v[98:113], v[212:215], v[142:145], v[98:113]

.LBB0_887:
	v_exp_f32_e32 v82, v82
	v_exp_f32_e32 v83, v83
	v_exp_f32_e32 v50, v50
	v_exp_f32_e32 v51, v51
	v_exp_f32_e32 v84, v84
	v_exp_f32_e32 v85, v85
	v_exp_f32_e32 v52, v52
	v_exp_f32_e32 v53, v53
	v_exp_f32_e32 v86, v86
	v_exp_f32_e32 v87, v87
	v_exp_f32_e32 v54, v54
	v_exp_f32_e32 v55, v55
	v_exp_f32_e32 v88, v88
	v_exp_f32_e32 v89, v89
	v_exp_f32_e32 v56, v56
	v_exp_f32_e32 v57, v57
	v_exp_f32_e32 v90, v90
	v_exp_f32_e32 v91, v91
	v_exp_f32_e32 v58, v58
	v_exp_f32_e32 v59, v59
	v_pk_add_f32 v[194:195], v[84:85], v[82:83]
	v_pk_add_f32 v[196:197], v[52:53], v[50:51]
	v_exp_f32_e32 v92, v92
	v_exp_f32_e32 v93, v93
	v_exp_f32_e32 v60, v60
	v_exp_f32_e32 v61, v61
	v_pk_add_f32 v[194:195], v[86:87], v[194:195]
	v_pk_add_f32 v[196:197], v[54:55], v[196:197]
	v_pk_add_f32 v[194:195], v[88:89], v[194:195]
	v_pk_add_f32 v[196:197], v[56:57], v[196:197]
	v_pk_add_f32 v[194:195], v[90:91], v[194:195]
	v_pk_add_f32 v[196:197], v[58:59], v[196:197]
	v_pk_add_f32 v[208:209], v[92:93], v[194:195]
	v_pk_add_f32 v[210:211], v[60:61], v[196:197]
	v_exp_f32_e32 v94, v94
	v_exp_f32_e32 v95, v95
	v_exp_f32_e32 v62, v62
	v_exp_f32_e32 v63, v63
	v_cvt_pk_f16_f32 v194, v82, v83
	v_cvt_pk_f16_f32 v195, v84, v85
	v_cvt_pk_f16_f32 v196, v86, v87
	v_cvt_pk_f16_f32 v197, v88, v89
	v_exp_f32_e32 v96, v96
	v_exp_f32_e32 v97, v97
	s_waitcnt lgkmcnt(0)
	v_mfma_f32_32x32x16_f16 v[2:17], v[158:161], v[194:197], v[2:17]
	v_exp_f32_e32 v64, v64
	v_exp_f32_e32 v65, v65
	v_pk_add_f32 v[158:159], v[94:95], v[208:209]
	v_pk_add_f32 v[160:161], v[62:63], v[210:211]
	v_pk_add_f32 v[158:159], v[96:97], v[158:159]
	v_pk_add_f32 v[160:161], v[64:65], v[160:161]
	v_mfma_f32_32x32x16_f16 v[18:33], v[154:157], v[194:197], v[18:33]
	v_add_f32_e64 v158, v160, v158
	v_add_f32_e64 v159, v161, v159
	v_cvt_pk_f16_f32 v154, v90, v91
	v_add_f32_e32 v208, v158, v159
	v_add_f32_e32 v183, v183, v208
	v_cvt_pk_f16_f32 v155, v92, v93
	v_cvt_pk_f16_f32 v156, v94, v95
	v_cvt_pk_f16_f32 v157, v96, v97
	v_mfma_f32_32x32x16_f16 v[34:49], v[150:153], v[194:197], v[34:49]
	v_cvt_pk_f16_f32 v158, v50, v51
	v_cvt_pk_f16_f32 v159, v52, v53
	v_cvt_pk_f16_f32 v160, v54, v55
	v_cvt_pk_f16_f32 v161, v56, v57
	v_cvt_pk_f16_f32 v150, v58, v59
	v_cvt_pk_f16_f32 v151, v60, v61
	v_cvt_pk_f16_f32 v152, v62, v63
	v_mfma_f32_32x32x16_f16 v[66:81], v[146:149], v[194:197], v[66:81]
	v_cvt_pk_f16_f32 v153, v64, v65
	s_and_b64 vcc, exec, s[34:35]
	ds_read_b64_tr_b16 v[146:147], v191 offset:12288
	ds_read_b64_tr_b16 v[148:149], v192 offset:12288
	ds_read_b64_tr_b16 v[208:209], v190 offset:12288
	ds_read_b64_tr_b16 v[210:211], v185 offset:12288
	ds_read_b64_tr_b16 v[212:213], v188 offset:12288
	ds_read_b64_tr_b16 v[214:215], v186 offset:12288
	ds_read_b64_tr_b16 v[216:217], v189 offset:12288
	ds_read_b64_tr_b16 v[218:219], v187 offset:12288
	ds_read_b64_tr_b16 v[220:221], v191 offset:16384
	ds_read_b64_tr_b16 v[222:223], v192 offset:16384
	s_waitcnt lgkmcnt(8)
	v_mfma_f32_32x32x16_f16 v[2:17], v[146:149], v[154:157], v[2:17]
	ds_read_b64_tr_b16 v[224:225], v190 offset:16384
	ds_read_b64_tr_b16 v[226:227], v185 offset:16384
	s_waitcnt lgkmcnt(8)
	v_mfma_f32_32x32x16_f16 v[18:33], v[208:211], v[154:157], v[18:33]
	ds_read_b64_tr_b16 v[146:147], v188 offset:16384
	ds_read_b64_tr_b16 v[148:149], v186 offset:16384
	s_waitcnt lgkmcnt(8)
	v_mfma_f32_32x32x16_f16 v[34:49], v[212:215], v[154:157], v[34:49]
	ds_read_b64_tr_b16 v[208:209], v189 offset:16384
	ds_read_b64_tr_b16 v[210:211], v187 offset:16384
	s_waitcnt lgkmcnt(8)
	v_mfma_f32_32x32x16_f16 v[66:81], v[216:219], v[154:157], v[66:81]
	ds_read_b64_tr_b16 v[212:213], v191 offset:20480
	ds_read_b64_tr_b16 v[214:215], v192 offset:20480
	s_waitcnt lgkmcnt(8)
	v_mfma_f32_32x32x16_f16 v[2:17], v[220:223], v[158:161], v[2:17]
	ds_read_b64_tr_b16 v[216:217], v190 offset:20480
	ds_read_b64_tr_b16 v[218:219], v185 offset:20480
	s_waitcnt lgkmcnt(8)
	v_mfma_f32_32x32x16_f16 v[18:33], v[224:227], v[158:161], v[18:33]
	ds_read_b64_tr_b16 v[220:221], v188 offset:20480
	ds_read_b64_tr_b16 v[222:223], v186 offset:20480
	s_waitcnt lgkmcnt(8)
	v_mfma_f32_32x32x16_f16 v[34:49], v[146:149], v[158:161], v[34:49]
	ds_read_b64_tr_b16 v[224:225], v189 offset:20480
	ds_read_b64_tr_b16 v[226:227], v187 offset:20480
	s_waitcnt lgkmcnt(8)
	v_mfma_f32_32x32x16_f16 v[66:81], v[208:211], v[158:161], v[66:81]
	s_waitcnt lgkmcnt(6)
	v_mfma_f32_32x32x16_f16 v[2:17], v[212:215], v[150:153], v[2:17]
	s_waitcnt lgkmcnt(4)
	v_mfma_f32_32x32x16_f16 v[18:33], v[216:219], v[150:153], v[18:33]
	s_waitcnt lgkmcnt(2)
	v_mfma_f32_32x32x16_f16 v[34:49], v[220:223], v[150:153], v[34:49]
	s_waitcnt lgkmcnt(0)
	v_mfma_f32_32x32x16_f16 v[66:81], v[224:227], v[150:153], v[66:81]
	v_mov_b32_e32 v146, 0
	s_cbranch_vccnz .LBB0_891
	s_mov_b32 s28, 0x41000000
	v_cmp_lg_f32_e64 s[34:35], s1, v193
	v_cmp_lt_f32_e32 vcc, s28, v193
	s_and_b64 s[30:31], s[30:31], s[34:35]
	s_or_b64 s[30:31], vcc, s[30:31]
	v_cndmask_b32_e64 v146, 0, 1, s[30:31]
	v_cmp_ne_u32_e32 vcc, 0, v146
	s_cbranch_vccz .LBB0_890
	v_add_f32_e32 v146, v184, v193
	v_max_f32_e32 v147, v172, v172
	v_max_f32_e32 v172, v147, v146
	v_cmp_neq_f32_e32 vcc, s1, v172
	s_nop 1
	v_cndmask_b32_e32 v146, 0, v172, vcc
	v_sub_f32_e32 v146, v146, v184
	v_exp_f32_e64 v148, -v146
	s_nop 0
	v_pk_mul_f32 v[16:17], v[148:149], v[16:17] op_sel_hi:[0,1]
	v_pk_mul_f32 v[14:15], v[148:149], v[14:15] op_sel_hi:[0,1]
	v_pk_mul_f32 v[12:13], v[148:149], v[12:13] op_sel_hi:[0,1]
	v_pk_mul_f32 v[10:11], v[148:149], v[10:11] op_sel_hi:[0,1]
	v_pk_mul_f32 v[8:9], v[148:149], v[8:9] op_sel_hi:[0,1]
	v_pk_mul_f32 v[6:7], v[148:149], v[6:7] op_sel_hi:[0,1]
	v_pk_mul_f32 v[4:5], v[148:149], v[4:5] op_sel_hi:[0,1]
	v_pk_mul_f32 v[2:3], v[148:149], v[2:3] op_sel_hi:[0,1]
	v_pk_mul_f32 v[32:33], v[148:149], v[32:33] op_sel_hi:[0,1]
	v_pk_mul_f32 v[30:31], v[148:149], v[30:31] op_sel_hi:[0,1]
	v_pk_mul_f32 v[28:29], v[148:149], v[28:29] op_sel_hi:[0,1]
	v_pk_mul_f32 v[26:27], v[148:149], v[26:27] op_sel_hi:[0,1]
	v_pk_mul_f32 v[24:25], v[148:149], v[24:25] op_sel_hi:[0,1]
	v_pk_mul_f32 v[22:23], v[148:149], v[22:23] op_sel_hi:[0,1]
	v_pk_mul_f32 v[20:21], v[148:149], v[20:21] op_sel_hi:[0,1]
	v_pk_mul_f32 v[18:19], v[148:149], v[18:19] op_sel_hi:[0,1]
	v_pk_mul_f32 v[48:49], v[148:149], v[48:49] op_sel_hi:[0,1]
	v_pk_mul_f32 v[46:47], v[148:149], v[46:47] op_sel_hi:[0,1]
	v_pk_mul_f32 v[44:45], v[148:149], v[44:45] op_sel_hi:[0,1]
	v_pk_mul_f32 v[42:43], v[148:149], v[42:43] op_sel_hi:[0,1]
	v_pk_mul_f32 v[40:41], v[148:149], v[40:41] op_sel_hi:[0,1]
	v_pk_mul_f32 v[38:39], v[148:149], v[38:39] op_sel_hi:[0,1]
	v_pk_mul_f32 v[36:37], v[148:149], v[36:37] op_sel_hi:[0,1]
	v_pk_mul_f32 v[34:35], v[148:149], v[34:35] op_sel_hi:[0,1]
	v_pk_mul_f32 v[80:81], v[148:149], v[80:81] op_sel_hi:[0,1]
	v_pk_mul_f32 v[78:79], v[148:149], v[78:79] op_sel_hi:[0,1]
	v_pk_mul_f32 v[76:77], v[148:149], v[76:77] op_sel_hi:[0,1]
	v_pk_mul_f32 v[74:75], v[148:149], v[74:75] op_sel_hi:[0,1]
	v_pk_mul_f32 v[72:73], v[148:149], v[72:73] op_sel_hi:[0,1]
	v_pk_mul_f32 v[70:71], v[148:149], v[70:71] op_sel_hi:[0,1]
	v_pk_mul_f32 v[68:69], v[148:149], v[68:69] op_sel_hi:[0,1]
	v_pk_mul_f32 v[66:67], v[148:149], v[66:67] op_sel_hi:[0,1]
	v_mul_f32_e32 v183, v183, v148
	s_branch .LBB0_891

.LBB0_896:
	s_cmp_ge_u32 s42, s90
	s_cbranch_scc1 .LBB0_910
	s_cmp_lt_u32 s44, s90
	v_cmp_eq_f32_e64 s[30:31], s1, v172
	s_cselect_b64 s[40:41], -1, 0
	s_cmp_ge_u32 s44, s90
	v_cndmask_b32_e64 v184, v172, 0, s[30:31]
	s_cbranch_scc1 .LBB0_899
	s_mul_i32 s34, s45, 0x6000
	v_add_u32_e32 v147, s34, v168
	ds_read_b128 v[148:151], v147
	v_xor_b32_e32 v50, 0x80000000, v184
	v_mov_b32_e32 v51, v50
	v_mov_b64_e32 v[52:53], v[50:51]
	v_mov_b64_e32 v[54:55], v[50:51]
	v_mov_b64_e32 v[56:57], v[50:51]
	v_mov_b64_e32 v[58:59], v[50:51]
	v_mov_b64_e32 v[60:61], v[50:51]
	v_mov_b64_e32 v[62:63], v[50:51]
	v_mov_b64_e32 v[64:65], v[50:51]
	ds_read_b128 v[152:155], v147 offset:4096
	v_add_u32_e32 v147, s34, v169
	ds_read_b128 v[156:159], v147
	ds_read_b128 v[188:191], v147 offset:4096
	v_add_u32_e32 v147, s34, v170
	ds_read_b128 v[192:195], v147
	ds_read_b128 v[196:199], v147 offset:4096
	v_add_u32_e32 v147, s34, v171
	ds_read_b128 v[208:211], v147
	ds_read_b128 v[212:215], v147 offset:4096
	s_waitcnt lgkmcnt(7)
	s_nop 0
	v_mfma_f32_32x32x16_f16 v[82:97], v[148:151], v[130:133], v[50:65]
	s_waitcnt lgkmcnt(6)
	v_mfma_f32_32x32x16_f16 v[50:65], v[152:155], v[130:133], v[50:65]
	s_waitcnt lgkmcnt(5)
	v_mfma_f32_32x32x16_f16 v[82:97], v[156:159], v[134:137], v[82:97]
	s_waitcnt lgkmcnt(4)
	v_mfma_f32_32x32x16_f16 v[50:65], v[188:191], v[134:137], v[50:65]
	s_waitcnt lgkmcnt(3)
	v_mfma_f32_32x32x16_f16 v[82:97], v[192:195], v[138:141], v[82:97]
	s_waitcnt lgkmcnt(2)
	v_mfma_f32_32x32x16_f16 v[50:65], v[196:199], v[138:141], v[50:65]
	s_waitcnt lgkmcnt(1)
	v_mfma_f32_32x32x16_f16 v[82:97], v[208:211], v[142:145], v[82:97]
	s_waitcnt lgkmcnt(0)
	v_mfma_f32_32x32x16_f16 v[50:65], v[212:215], v[142:145], v[50:65]

.LBB0_905:
	v_exp_f32_e32 v114, v114
	v_exp_f32_e32 v115, v115
	v_exp_f32_e32 v98, v98
	v_exp_f32_e32 v99, v99
	v_exp_f32_e32 v116, v116
	v_exp_f32_e32 v117, v117
	v_exp_f32_e32 v100, v100
	v_exp_f32_e32 v101, v101
	v_exp_f32_e32 v118, v118
	v_exp_f32_e32 v119, v119
	v_exp_f32_e32 v102, v102
	v_exp_f32_e32 v103, v103
	v_exp_f32_e32 v120, v120
	v_exp_f32_e32 v121, v121
	v_exp_f32_e32 v104, v104
	v_exp_f32_e32 v105, v105
	v_exp_f32_e32 v122, v122
	v_exp_f32_e32 v123, v123
	v_exp_f32_e32 v106, v106
	v_exp_f32_e32 v107, v107
	v_pk_add_f32 v[194:195], v[116:117], v[114:115]
	v_pk_add_f32 v[196:197], v[100:101], v[98:99]
	v_exp_f32_e32 v124, v124
	v_exp_f32_e32 v125, v125
	v_exp_f32_e32 v108, v108
	v_exp_f32_e32 v109, v109
	v_pk_add_f32 v[194:195], v[118:119], v[194:195]
	v_pk_add_f32 v[196:197], v[102:103], v[196:197]
	v_pk_add_f32 v[194:195], v[120:121], v[194:195]
	v_pk_add_f32 v[196:197], v[104:105], v[196:197]
	v_pk_add_f32 v[194:195], v[122:123], v[194:195]
	v_pk_add_f32 v[196:197], v[106:107], v[196:197]
	v_pk_add_f32 v[208:209], v[124:125], v[194:195]
	v_pk_add_f32 v[210:211], v[108:109], v[196:197]
	v_exp_f32_e32 v126, v126
	v_exp_f32_e32 v127, v127
	v_exp_f32_e32 v110, v110
	v_exp_f32_e32 v111, v111
	v_cvt_pk_f16_f32 v194, v114, v115
	v_cvt_pk_f16_f32 v195, v116, v117
	v_cvt_pk_f16_f32 v196, v118, v119
	v_cvt_pk_f16_f32 v197, v120, v121
	v_exp_f32_e32 v128, v128
	v_exp_f32_e32 v129, v129
	s_waitcnt lgkmcnt(0)
	v_mfma_f32_32x32x16_f16 v[2:17], v[158:161], v[194:197], v[2:17]
	v_exp_f32_e32 v112, v112
	v_exp_f32_e32 v113, v113
	v_pk_add_f32 v[158:159], v[126:127], v[208:209]
	v_pk_add_f32 v[160:161], v[110:111], v[210:211]
	v_pk_add_f32 v[158:159], v[128:129], v[158:159]
	v_pk_add_f32 v[160:161], v[112:113], v[160:161]
	v_mfma_f32_32x32x16_f16 v[18:33], v[154:157], v[194:197], v[18:33]
	v_add_f32_e64 v158, v158, v160
	v_add_f32_e64 v159, v159, v161
	v_cvt_pk_f16_f32 v154, v122, v123
	v_add_f32_e32 v208, v158, v159
	v_add_f32_e32 v183, v183, v208
	v_cvt_pk_f16_f32 v155, v124, v125
	v_cvt_pk_f16_f32 v156, v126, v127
	v_cvt_pk_f16_f32 v157, v128, v129
	v_mfma_f32_32x32x16_f16 v[34:49], v[150:153], v[194:197], v[34:49]
	v_cvt_pk_f16_f32 v158, v98, v99
	v_cvt_pk_f16_f32 v159, v100, v101
	v_cvt_pk_f16_f32 v160, v102, v103
	v_cvt_pk_f16_f32 v161, v104, v105
	v_cvt_pk_f16_f32 v150, v106, v107
	v_cvt_pk_f16_f32 v151, v108, v109
	v_cvt_pk_f16_f32 v152, v110, v111
	v_mfma_f32_32x32x16_f16 v[66:81], v[146:149], v[194:197], v[66:81]
	v_cvt_pk_f16_f32 v153, v112, v113
	s_and_b64 vcc, exec, s[34:35]
	ds_read_b64_tr_b16 v[146:147], v191 offset:12288
	ds_read_b64_tr_b16 v[148:149], v192 offset:12288
	ds_read_b64_tr_b16 v[208:209], v190 offset:12288
	ds_read_b64_tr_b16 v[210:211], v185 offset:12288
	ds_read_b64_tr_b16 v[212:213], v188 offset:12288
	ds_read_b64_tr_b16 v[214:215], v186 offset:12288
	ds_read_b64_tr_b16 v[216:217], v189 offset:12288
	ds_read_b64_tr_b16 v[218:219], v187 offset:12288
	ds_read_b64_tr_b16 v[220:221], v191 offset:16384
	ds_read_b64_tr_b16 v[222:223], v192 offset:16384
	s_waitcnt lgkmcnt(8)
	v_mfma_f32_32x32x16_f16 v[2:17], v[146:149], v[154:157], v[2:17]
	ds_read_b64_tr_b16 v[224:225], v190 offset:16384
	ds_read_b64_tr_b16 v[226:227], v185 offset:16384
	s_waitcnt lgkmcnt(8)
	v_mfma_f32_32x32x16_f16 v[18:33], v[208:211], v[154:157], v[18:33]
	ds_read_b64_tr_b16 v[146:147], v188 offset:16384
	ds_read_b64_tr_b16 v[148:149], v186 offset:16384
	s_waitcnt lgkmcnt(8)
	v_mfma_f32_32x32x16_f16 v[34:49], v[212:215], v[154:157], v[34:49]
	ds_read_b64_tr_b16 v[208:209], v189 offset:16384
	ds_read_b64_tr_b16 v[210:211], v187 offset:16384
	s_waitcnt lgkmcnt(8)
	v_mfma_f32_32x32x16_f16 v[66:81], v[216:219], v[154:157], v[66:81]
	ds_read_b64_tr_b16 v[212:213], v191 offset:20480
	ds_read_b64_tr_b16 v[214:215], v192 offset:20480
	s_waitcnt lgkmcnt(8)
	v_mfma_f32_32x32x16_f16 v[2:17], v[220:223], v[158:161], v[2:17]
	ds_read_b64_tr_b16 v[216:217], v190 offset:20480
	ds_read_b64_tr_b16 v[218:219], v185 offset:20480
	s_waitcnt lgkmcnt(8)
	v_mfma_f32_32x32x16_f16 v[18:33], v[224:227], v[158:161], v[18:33]
	ds_read_b64_tr_b16 v[220:221], v188 offset:20480
	ds_read_b64_tr_b16 v[222:223], v186 offset:20480
	s_waitcnt lgkmcnt(8)
	v_mfma_f32_32x32x16_f16 v[34:49], v[146:149], v[158:161], v[34:49]
	ds_read_b64_tr_b16 v[224:225], v189 offset:20480
	ds_read_b64_tr_b16 v[226:227], v187 offset:20480
	s_waitcnt lgkmcnt(8)
	v_mfma_f32_32x32x16_f16 v[66:81], v[208:211], v[158:161], v[66:81]
	s_waitcnt lgkmcnt(6)
	v_mfma_f32_32x32x16_f16 v[2:17], v[212:215], v[150:153], v[2:17]
	s_waitcnt lgkmcnt(4)
	v_mfma_f32_32x32x16_f16 v[18:33], v[216:219], v[150:153], v[18:33]
	s_waitcnt lgkmcnt(2)
	v_mfma_f32_32x32x16_f16 v[34:49], v[220:223], v[150:153], v[34:49]
	s_waitcnt lgkmcnt(0)
	v_mfma_f32_32x32x16_f16 v[66:81], v[224:227], v[150:153], v[66:81]
	v_mov_b32_e32 v146, 0
	s_cbranch_vccnz .LBB0_910
	s_mov_b32 s26, 0x41000000
	v_cmp_lg_f32_e64 s[34:35], s1, v193
	v_cmp_lt_f32_e32 vcc, s26, v193
	s_and_b64 s[30:31], s[30:31], s[34:35]
	s_or_b64 s[30:31], vcc, s[30:31]
	v_cndmask_b32_e64 v146, 0, 1, s[30:31]
	v_cmp_ne_u32_e32 vcc, 0, v146
	s_cbranch_vccz .LBB0_909
	v_add_f32_e32 v146, v184, v193
	v_max_f32_e32 v147, v172, v172
	v_max_f32_e32 v172, v147, v146
	v_cmp_neq_f32_e32 vcc, s1, v172
	s_nop 1
	v_cndmask_b32_e32 v146, 0, v172, vcc
	v_sub_f32_e32 v146, v146, v184
	v_exp_f32_e64 v148, -v146
	s_nop 0
	v_pk_mul_f32 v[16:17], v[148:149], v[16:17] op_sel_hi:[0,1]
	v_pk_mul_f32 v[14:15], v[148:149], v[14:15] op_sel_hi:[0,1]
	v_pk_mul_f32 v[12:13], v[148:149], v[12:13] op_sel_hi:[0,1]
	v_pk_mul_f32 v[10:11], v[148:149], v[10:11] op_sel_hi:[0,1]
	v_pk_mul_f32 v[8:9], v[148:149], v[8:9] op_sel_hi:[0,1]
	v_pk_mul_f32 v[6:7], v[148:149], v[6:7] op_sel_hi:[0,1]
	v_pk_mul_f32 v[4:5], v[148:149], v[4:5] op_sel_hi:[0,1]
	v_pk_mul_f32 v[2:3], v[148:149], v[2:3] op_sel_hi:[0,1]
	v_pk_mul_f32 v[32:33], v[148:149], v[32:33] op_sel_hi:[0,1]
	v_pk_mul_f32 v[30:31], v[148:149], v[30:31] op_sel_hi:[0,1]
	v_pk_mul_f32 v[28:29], v[148:149], v[28:29] op_sel_hi:[0,1]
	v_pk_mul_f32 v[26:27], v[148:149], v[26:27] op_sel_hi:[0,1]
	v_pk_mul_f32 v[24:25], v[148:149], v[24:25] op_sel_hi:[0,1]
	v_pk_mul_f32 v[22:23], v[148:149], v[22:23] op_sel_hi:[0,1]
	v_pk_mul_f32 v[20:21], v[148:149], v[20:21] op_sel_hi:[0,1]
	v_pk_mul_f32 v[18:19], v[148:149], v[18:19] op_sel_hi:[0,1]
	v_pk_mul_f32 v[48:49], v[148:149], v[48:49] op_sel_hi:[0,1]
	v_pk_mul_f32 v[46:47], v[148:149], v[46:47] op_sel_hi:[0,1]
	v_pk_mul_f32 v[44:45], v[148:149], v[44:45] op_sel_hi:[0,1]
	v_pk_mul_f32 v[42:43], v[148:149], v[42:43] op_sel_hi:[0,1]
	v_pk_mul_f32 v[40:41], v[148:149], v[40:41] op_sel_hi:[0,1]
	v_pk_mul_f32 v[38:39], v[148:149], v[38:39] op_sel_hi:[0,1]
	v_pk_mul_f32 v[36:37], v[148:149], v[36:37] op_sel_hi:[0,1]
	v_pk_mul_f32 v[34:35], v[148:149], v[34:35] op_sel_hi:[0,1]
	v_pk_mul_f32 v[80:81], v[148:149], v[80:81] op_sel_hi:[0,1]
	v_pk_mul_f32 v[78:79], v[148:149], v[78:79] op_sel_hi:[0,1]
	v_pk_mul_f32 v[76:77], v[148:149], v[76:77] op_sel_hi:[0,1]
	v_pk_mul_f32 v[74:75], v[148:149], v[74:75] op_sel_hi:[0,1]
	v_pk_mul_f32 v[72:73], v[148:149], v[72:73] op_sel_hi:[0,1]
	v_pk_mul_f32 v[70:71], v[148:149], v[70:71] op_sel_hi:[0,1]
	v_pk_mul_f32 v[68:69], v[148:149], v[68:69] op_sel_hi:[0,1]
	v_pk_mul_f32 v[66:67], v[148:149], v[66:67] op_sel_hi:[0,1]
	v_mul_f32_e32 v183, v183, v148
	s_branch .LBB0_910

; #define LAS __attribute__((address_space(3)))
; __device__ __forceinline__ float half_sum(float x) { const auto rr = __builtin_amdgcn_permlane32_swap(__float_as_uint(x), __float_as_uint(x), false, false); return __uint_as_float(rr[0]) + __uint_as_float(rr[1]); }
; __global__ void __launch_bounds__(NWAVES * 64, 2) mega_fwd(Args args) {
;     ...
;                   float gate[8];
; #pragma unroll
;                   for (int n = 0; n < 8; ++n) { float g = 0.f;
; #pragma unroll
;                     for (int d0 = 0; d0 < 4; ++d0) { const f32x4 k0 = *(const LAS f32x4*)(kmL + n * 64 + 8 * hi + 16 * d0), k1 = *(const LAS f32x4*)(kmL + n * 64 + 8 * hi + 16 * d0 + 4);
;                         g += ((float)qv[d0][0] * k0.x + (float)qv[d0][1] * k0.y) + ((float)qv[d0][2] * k0.z + (float)qv[d0][3] * k0.w) + ((float)qv[d0][4] * k1.x + (float)qv[d0][5] * k1.y) + ((float)qv[d0][6] * k1.z + (float)qv[d0][7] * k1.w); }
;                     g = fa::half_sum(g);
;                     gate[n] = (n < qb) ? g : -INFINITY; }
; #pragma unroll
;                   for (int pick = 0; pick < 3; ++pick) { float best = -INFINITY; int bi = -1;
; #pragma unroll
;                     for (int n = 0; n < 8; ++n) if (!((selb >> n) & 1u) && gate[n] > best) { best = gate[n]; bi = n; }
;                     if (bi >= 0) selb |= 1u << bi; } }
.LBB0_956:
	s_cmp_eq_u32 s61, 7
	s_cselect_b64 vcc, -1, 0
	s_cmp_gt_u32 s58, 1
	s_cselect_b64 s[30:31], -1, 0
	s_cmp_gt_u32 s58, 2
	s_cselect_b64 s[34:35], -1, 0
	s_cmp_gt_u32 s58, 3
	s_cselect_b64 s[36:37], -1, 0
	s_cmp_gt_u32 s58, 4
	v_add_f32_e32 v10, v46, v47
	v_add_f32_e32 v11, v64, v65
	s_cselect_b64 s[38:39], -1, 0
	s_cmp_gt_u32 s58, 5
	v_add_f32_e32 v2, v2, v8
	v_cndmask_b32_e32 v8, v10, v233, vcc
	v_cndmask_b32_e64 v10, v233, v11, s[30:31]
	v_add_f32_e32 v4, v4, v9
	s_cselect_b64 s[30:31], -1, 0
	s_cmp_eq_u32 s61, 0
	v_cndmask_b32_e64 v4, v233, v4, s[30:31]
	v_add_f32_e32 v6, v6, v7
	s_cselect_b64 s[30:31], -1, 0
	v_cndmask_b32_e64 v6, v233, v6, s[30:31]
	v_cmp_nlg_f32_e64 s[30:31], s1, v8
	v_add_f32_e32 v12, v48, v49
	v_cndmask_b32_e64 v11, v233, v12, s[34:35]
	v_cndmask_b32_e64 v7, v8, v233, s[30:31]
	v_cmp_gt_f32_e64 s[34:35], v10, v7
	v_cndmask_b32_e64 v9, 0, -1, s[30:31]
	v_add_f32_e32 v13, v26, v27
	v_cndmask_b32_e64 v7, v7, v10, s[34:35]
	v_cndmask_b32_e64 v9, v9, 1, s[34:35]
	v_cmp_gt_f32_e64 s[34:35], v11, v7
	v_cndmask_b32_e64 v12, v233, v13, s[36:37]
	v_cndmask_b32_e64 v2, v233, v2, s[38:39]
	v_cndmask_b32_e64 v7, v7, v11, s[34:35]
	v_cndmask_b32_e64 v9, v9, 2, s[34:35]
	v_cmp_gt_f32_e64 s[34:35], v12, v7
	v_readlane_b32 s28, v253, 13
	v_lshrrev_b32_e32 v34, 1, v160
	v_cndmask_b32_e64 v7, v7, v12, s[34:35]
	v_cndmask_b32_e64 v9, v9, 3, s[34:35]
	v_cmp_gt_f32_e64 s[34:35], v2, v7
	v_lshlrev_b32_e32 v35, 7, v161
	s_mov_b32 m0, s85
	v_cndmask_b32_e64 v7, v7, v2, s[34:35]
	v_cndmask_b32_e64 v9, v9, 4, s[34:35]
	v_cmp_gt_f32_e64 s[34:35], v4, v7
	v_add_u32_e32 v40, 2, v132
	v_bitop3_b32 v40, v40, v34, 7 bitop3:0x78
	v_cndmask_b32_e64 v7, v7, v4, s[34:35]
	v_cndmask_b32_e64 v9, v9, 5, s[34:35]
	v_cmp_ngt_f32_e64 s[34:35], v6, v7
	v_lshl_add_u32 v135, v40, 4, v35
	v_add_u32_e32 v40, 4, v132
	v_cndmask_b32_e64 v7, 6, v9, s[34:35]
	v_lshlrev_b32_e64 v9, v7, 1
	v_cmp_lt_i32_e64 s[34:35], -1, v7
	v_bitop3_b32 v40, v40, v34, 7 bitop3:0x78
	v_lshl_add_u32 v136, v40, 4, v35
	v_cndmask_b32_e64 v7, 0, v9, s[34:35]
	v_and_b32_e32 v9, 1, v7
	v_cmp_eq_u32_e64 s[34:35], 1, v9
	s_or_b64 s[34:35], s[34:35], s[30:31]
	v_and_b32_e32 v14, 2, v7
	v_cndmask_b32_e64 v9, v8, v233, s[34:35]
	v_cndmask_b32_e64 v13, 0, -1, s[34:35]
	v_cmp_eq_u32_e64 s[34:35], 0, v14
	v_cmp_gt_f32_e64 s[36:37], v10, v9
	s_and_b64 s[34:35], s[34:35], s[36:37]
	v_cndmask_b32_e64 v9, v9, v10, s[34:35]
	v_and_b32_e32 v14, 4, v7
	v_cndmask_b32_e64 v13, v13, 1, s[34:35]
	v_cmp_eq_u32_e64 s[34:35], 0, v14
	v_cmp_gt_f32_e64 s[36:37], v11, v9
	s_and_b64 s[34:35], s[34:35], s[36:37]
	v_cndmask_b32_e64 v9, v9, v11, s[34:35]
	v_and_b32_e32 v14, 8, v7
	v_cndmask_b32_e64 v13, v13, 2, s[34:35]
	v_cmp_eq_u32_e64 s[34:35], 0, v14
	v_cmp_gt_f32_e64 s[36:37], v12, v9
	s_and_b64 s[34:35], s[34:35], s[36:37]
	v_cndmask_b32_e64 v9, v9, v12, s[34:35]
	v_and_b32_e32 v14, 16, v7
	v_cndmask_b32_e64 v13, v13, 3, s[34:35]
	v_cmp_eq_u32_e64 s[34:35], 0, v14
	v_cmp_gt_f32_e64 s[36:37], v2, v9
	s_and_b64 s[34:35], s[34:35], s[36:37]
	v_cndmask_b32_e64 v9, v9, v2, s[34:35]
	v_and_b32_e32 v14, 32, v7
	v_cndmask_b32_e64 v13, v13, 4, s[34:35]
	v_cmp_eq_u32_e64 s[34:35], 0, v14
	v_cmp_gt_f32_e64 s[36:37], v4, v9
	s_and_b64 s[34:35], s[34:35], s[36:37]
	v_cndmask_b32_e64 v9, v9, v4, s[34:35]
	v_and_b32_e32 v14, 64, v7
	v_cndmask_b32_e64 v13, v13, 5, s[34:35]
	v_cmp_eq_u32_e64 s[34:35], 0, v14
	v_cmp_gt_f32_e64 s[36:37], v6, v9
	s_and_b64 s[34:35], s[34:35], s[36:37]
	v_cndmask_b32_e64 v9, v13, 6, s[34:35]
	v_lshlrev_b32_e64 v13, v9, 1
	v_cmp_lt_i32_e64 s[34:35], -1, v9
	s_mul_i32 s36, s59, 0xa00
	v_add_u32_e32 v40, 6, v132
	v_cndmask_b32_e64 v9, 0, v13, s[34:35]
	v_or_b32_e32 v7, v9, v7
	v_and_b32_e32 v9, 1, v7
	v_cmp_eq_u32_e64 s[34:35], 1, v9
	s_or_b64 s[30:31], s[34:35], s[30:31]
	v_cndmask_b32_e64 v8, v8, v233, s[30:31]
	v_and_b32_e32 v13, 2, v7
	v_cndmask_b32_e64 v9, 0, -1, s[30:31]
	v_cmp_eq_u32_e64 s[30:31], 0, v13
	v_cmp_gt_f32_e64 s[34:35], v10, v8
	s_and_b64 s[30:31], s[30:31], s[34:35]
	v_cndmask_b32_e64 v8, v8, v10, s[30:31]
	v_and_b32_e32 v10, 4, v7
	v_cndmask_b32_e64 v9, v9, 1, s[30:31]
	v_cmp_eq_u32_e64 s[30:31], 0, v10
	v_cmp_gt_f32_e64 s[34:35], v11, v8
	s_and_b64 s[30:31], s[30:31], s[34:35]
	v_cndmask_b32_e64 v8, v8, v11, s[30:31]
	v_and_b32_e32 v10, 8, v7
	v_cndmask_b32_e64 v9, v9, 2, s[30:31]
	v_cmp_eq_u32_e64 s[30:31], 0, v10
	v_cmp_gt_f32_e64 s[34:35], v12, v8
	s_and_b64 s[30:31], s[30:31], s[34:35]
	v_cndmask_b32_e64 v8, v8, v12, s[30:31]
	v_and_b32_e32 v10, 16, v7
	v_cndmask_b32_e64 v9, v9, 3, s[30:31]
	v_cmp_eq_u32_e64 s[30:31], 0, v10
	v_cmp_gt_f32_e64 s[34:35], v2, v8
	s_and_b64 s[30:31], s[30:31], s[34:35]
	v_cndmask_b32_e64 v2, v8, v2, s[30:31]
	v_cndmask_b32_e64 v8, v9, 4, s[30:31]
	v_and_b32_e32 v9, 32, v7
	v_cmp_eq_u32_e64 s[30:31], 0, v9
	v_cmp_gt_f32_e64 s[34:35], v4, v2
	s_and_b64 s[30:31], s[30:31], s[34:35]
	v_cndmask_b32_e64 v2, v2, v4, s[30:31]
	v_cndmask_b32_e64 v4, v8, 5, s[30:31]
	v_and_b32_e32 v8, 64, v7
	v_cmp_eq_u32_e64 s[30:31], 0, v8
	v_cmp_gt_f32_e64 s[34:35], v6, v2
	s_and_b64 s[30:31], s[30:31], s[34:35]
	v_cndmask_b32_e64 v2, v4, 6, s[30:31]
; #define FA_WAITV(n) asm volatile("s_waitcnt vmcnt(%0)" :: "n"(n) : "memory")
; template <int DQK, int DV, int MODE, int S> ...
;     ...
; #pragma unroll
;     for (int t0 = 0; t0 < S - 1; ++t0) if (t0 < ntiles) FP_ISSUE(t0, t0);
;     f32x16 sa0, sa1, sb0, sb1; float dl;
;     if (ntiles >= S - 1) FA_WAITV(L::NPW * (S - 2)); else FA_WAITV(0);
;     __builtin_amdgcn_s_barrier(); asm volatile("" ::: "memory");
;     { float rmrel; FP_QK(sa0, sa1, 0, 0, 0.f); FP_PREP(sa0, sa1, 0); m = rmrel; dl = (m == -INFINITY) ? 0.f : m; }
	v_lshlrev_b32_e64 v4, v2, 1
	v_cmp_lt_i32_e64 s[30:31], -1, v2
	s_mul_i32 s35, s92, 0xd00000
	s_mul_hi_u32 s34, s92, 0xd00000
	v_cndmask_b32_e64 v2, 0, v4, s[30:31]
	s_add_u32 s37, s26, s35
	v_or_b32_e32 v133, v2, v7
	s_addc_u32 s38, s60, s34
	s_lshl_b32 s26, s62, 1
	v_add_u32_e32 v2, s28, v3
	s_add_u32 s30, s37, s26
	v_ashrrev_i32_e32 v3, 31, v2
	s_addc_u32 s31, s38, 0
	s_add_i32 s36, s36, 0x22400
	v_lshrrev_b32_e32 v3, 29, v3
	s_add_u32 s37, s37, s42
	v_add_u32_e32 v3, v2, v3
	s_addc_u32 s39, s38, s43
	v_ashrrev_i32_e32 v4, 3, v3
	v_and_b32_e32 v3, 0x1ffffff8, v3
	s_add_u32 s38, s37, s26
	s_movk_i32 s37, 0xd00
	v_sub_u32_e32 v2, v2, v3
	v_lshlrev_b32_e32 v3, 1, v4
	v_bitop3_b32 v2, v3, v2, 4 bitop3:0x6c
	v_mul_lo_u32 v3, v4, s37
	v_mul_lo_u32 v0, v0, s37
	v_lshl_add_u32 v2, v2, 3, v3
	v_bitop3_b32 v3, v34, v132, 7 bitop3:0x6c
	v_lshl_add_u32 v0, v5, 3, v0
	v_lshl_add_u32 v134, v3, 4, v35
	v_mov_b32_e32 v3, v1
	s_addc_u32 s39, s39, 0
	v_lshlrev_b64 v[4:5], 1, v[0:1]
	v_lshlrev_b64 v[130:131], 1, v[2:3]
	v_lshl_add_u64 v[6:7], s[38:39], 0, v[4:5]
	v_lshl_add_u64 v[2:3], s[30:31], 0, v[130:131]
	s_mov_b64 s[38:39], 0x1750
	v_lshl_add_u64 v[2:3], v[2:3], 0, s[38:39]
	s_add_u32 s38, s30, 0x69750
	s_addc_u32 s39, s31, 0
	s_add_u32 s37, s30, 0x69550
	s_addc_u32 s59, s31, 0
	s_and_b64 s[42:43], s[8:9], exec
	global_load_lds_dwordx4 v[6:7], off
	s_mov_b32 m0, s86
	s_cselect_b32 s43, s59, s39
	s_cselect_b32 s42, s37, s38
	global_load_lds_dwordx4 v[2:3], off
	v_lshl_add_u64 v[2:3], s[42:43], 0, v[4:5]
	s_add_i32 m0, s85, 0x4000
	v_bitop3_b32 v40, v40, v34, 7 bitop3:0x78
	global_load_lds_dwordx4 v[2:3], off
	s_add_i32 m0, s86, 0x4000
	v_lshl_add_u64 v[2:3], s[38:39], 0, v[130:131]
	s_add_u32 s38, s30, 0xd1750
	s_addc_u32 s39, s31, 0
	s_add_u32 s37, s30, 0xd1550
	s_addc_u32 s42, s31, 0
	s_and_b64 s[30:31], s[8:9], exec
	s_cselect_b32 s31, s42, s39
	s_cselect_b32 s30, s37, s38
	global_load_lds_dwordx4 v[2:3], off
	v_lshl_add_u64 v[2:3], s[30:31], 0, v[4:5]
	s_add_i32 m0, s85, 0x8000
	v_lshl_add_u32 v137, v40, 4, v35
	global_load_lds_dwordx4 v[2:3], off
	v_lshl_add_u64 v[2:3], s[38:39], 0, v[130:131]
	s_add_i32 m0, s86, 0x8000
	v_lshlrev_b32_e32 v35, 2, v132
	global_load_lds_dwordx4 v[2:3], off
	s_waitcnt vmcnt(4)
	s_barrier
	ds_read_b128 v[36:39], v134
	v_and_b32_e32 v2, 1, v133
	v_cmp_eq_u32_e64 s[30:31], 1, v2
	s_or_b64 vcc, vcc, s[30:31]
	v_cndmask_b32_e32 v2, v233, v230, vcc
	v_mov_b32_e32 v3, v2
	v_mov_b64_e32 v[4:5], v[2:3]
	v_mov_b64_e32 v[6:7], v[2:3]
	v_mov_b64_e32 v[8:9], v[2:3]
	v_mov_b64_e32 v[10:11], v[2:3]
	v_mov_b64_e32 v[12:13], v[2:3]
	v_mov_b64_e32 v[14:15], v[2:3]
	v_mov_b64_e32 v[16:17], v[2:3]
	s_cmpk_gt_u32 s45, 0xbe
	v_readlane_b32 s29, v253, 14
	s_waitcnt vmcnt(0) lgkmcnt(0)
	v_mfma_f32_32x32x16_f16 v[18:33], v[36:39], v[98:101], v[2:17]
	ds_read_b128 v[36:39], v134 offset:4096
	s_waitcnt lgkmcnt(0)
	v_mfma_f32_32x32x16_f16 v[2:17], v[36:39], v[98:101], v[2:17]
	ds_read_b128 v[36:39], v135
	s_waitcnt lgkmcnt(0)
	v_mfma_f32_32x32x16_f16 v[18:33], v[36:39], v[102:105], v[18:33]
	ds_read_b128 v[36:39], v135 offset:4096
	s_waitcnt lgkmcnt(0)
	v_mfma_f32_32x32x16_f16 v[2:17], v[36:39], v[102:105], v[2:17]
	ds_read_b128 v[36:39], v136
	s_waitcnt lgkmcnt(0)
	v_mfma_f32_32x32x16_f16 v[18:33], v[36:39], v[106:109], v[18:33]
	ds_read_b128 v[36:39], v136 offset:4096
	s_waitcnt lgkmcnt(0)
	v_mfma_f32_32x32x16_f16 v[2:17], v[36:39], v[106:109], v[2:17]
	ds_read_b128 v[36:39], v137
	s_waitcnt lgkmcnt(0)
	v_mfma_f32_32x32x16_f16 v[18:33], v[36:39], v[110:113], v[18:33]
	ds_read_b128 v[36:39], v137 offset:4096
	s_waitcnt lgkmcnt(0)
	v_mfma_f32_32x32x16_f16 v[2:17], v[36:39], v[110:113], v[2:17]
	v_or_b32_e32 v36, s45, v161
	v_sub_u32_e32 v37, v35, v36
	v_and_b32_e32 v36, 1, v37
	v_cmp_eq_u32_e32 vcc, 1, v36
	v_mov_b32_e32 v36, 0x500
	s_nop 0
	v_cndmask_b32_e32 v36, 0, v36, vcc
	s_cbranch_scc1 .LBB0_958
	v_and_b32_e32 v37, 0x3ffffffe, v37
	v_lshlrev_b32_e32 v37, 2, v37
	v_add3_u32 v37, s36, v36, v37
	ds_read2_b64 v[38:41], v37 offset0:112 offset1:113
	ds_read2_b64 v[42:45], v37 offset0:116 offset1:117
	ds_read2_b64 v[46:49], v37 offset0:120 offset1:121
	ds_read2_b64 v[50:53], v37 offset0:124 offset1:125
	ds_read2_b64 v[54:57], v37 offset0:128 offset1:129
	ds_read2_b64 v[58:61], v37 offset0:132 offset1:133
	ds_read2_b64 v[62:65], v37 offset0:136 offset1:137
	ds_read2_b64 v[66:69], v37 offset0:140 offset1:141
	s_waitcnt lgkmcnt(4)
	v_pk_add_f32 v[30:31], v[30:31], v[50:51]
	v_pk_add_f32 v[26:27], v[26:27], v[46:47]
	v_pk_add_f32 v[22:23], v[22:23], v[42:43]
	v_pk_add_f32 v[32:33], v[32:33], v[52:53]
	v_pk_add_f32 v[28:29], v[28:29], v[48:49]
	v_pk_add_f32 v[24:25], v[24:25], v[44:45]
	v_pk_add_f32 v[20:21], v[20:21], v[40:41]
	v_pk_add_f32 v[18:19], v[18:19], v[38:39]
	s_waitcnt lgkmcnt(0)
	v_pk_add_f32 v[14:15], v[14:15], v[66:67]
	v_pk_add_f32 v[10:11], v[10:11], v[62:63]
	v_pk_add_f32 v[6:7], v[6:7], v[58:59]
	v_pk_add_f32 v[16:17], v[16:17], v[68:69]
	v_pk_add_f32 v[12:13], v[12:13], v[64:65]
	v_pk_add_f32 v[8:9], v[8:9], v[60:61]
	v_pk_add_f32 v[4:5], v[4:5], v[56:57]
	v_pk_add_f32 v[2:3], v[2:3], v[54:55]

.LBB0_969:
	v_mov_b32_e32 v66, 0xff800000
	s_and_saveexec_b64 s[44:45], s[34:35]
	v_xor_b32_e32 v66, 0x80000000, v146
	s_or_b64 exec, exec, s[44:45]
	s_lshl_b32 s34, s65, 14
	v_add_u32_e32 v115, s34, v134
	ds_read_b128 v[116:119], v115
	v_mov_b32_e32 v67, v66
	v_mov_b64_e32 v[68:69], v[66:67]
	v_mov_b64_e32 v[70:71], v[66:67]
	v_mov_b64_e32 v[72:73], v[66:67]
	v_mov_b64_e32 v[74:75], v[66:67]
	v_mov_b64_e32 v[76:77], v[66:67]
	v_mov_b64_e32 v[78:79], v[66:67]
	v_mov_b64_e32 v[80:81], v[66:67]
	ds_read_b128 v[120:123], v115 offset:4096
	v_add_u32_e32 v115, s34, v135
	ds_read_b128 v[124:127], v115
	ds_read_b128 v[148:151], v115 offset:4096
	v_add_u32_e32 v115, s34, v136
	ds_read_b128 v[152:155], v115
	ds_read_b128 v[156:159], v115 offset:4096
	v_add_u32_e32 v115, s34, v137
	ds_read_b128 v[164:167], v115
	ds_read_b128 v[168:171], v115 offset:4096
	s_waitcnt lgkmcnt(7)
	s_nop 0
	v_mfma_f32_32x32x16_f16 v[82:97], v[116:119], v[98:101], v[66:81]
	s_waitcnt lgkmcnt(6)
	v_mfma_f32_32x32x16_f16 v[66:81], v[120:123], v[98:101], v[66:81]
	s_waitcnt lgkmcnt(5)
	v_mfma_f32_32x32x16_f16 v[82:97], v[124:127], v[102:105], v[82:97]
	s_waitcnt lgkmcnt(4)
	v_mfma_f32_32x32x16_f16 v[66:81], v[148:151], v[102:105], v[66:81]
	s_waitcnt lgkmcnt(3)
	v_mfma_f32_32x32x16_f16 v[82:97], v[152:155], v[106:109], v[82:97]
	s_waitcnt lgkmcnt(2)
	v_mfma_f32_32x32x16_f16 v[66:81], v[156:159], v[106:109], v[66:81]
	s_waitcnt lgkmcnt(1)
	v_mfma_f32_32x32x16_f16 v[82:97], v[164:167], v[110:113], v[82:97]
	s_waitcnt lgkmcnt(0)
	v_mfma_f32_32x32x16_f16 v[66:81], v[168:171], v[110:113], v[66:81]

.LBB0_978:
	v_exp_f32_e32 v18, v18
	v_exp_f32_e32 v19, v19
	v_exp_f32_e32 v2, v2
	v_exp_f32_e32 v3, v3
	v_exp_f32_e32 v20, v20
	v_exp_f32_e32 v21, v21
	v_exp_f32_e32 v4, v4
	v_exp_f32_e32 v5, v5
	v_exp_f32_e32 v22, v22
	v_exp_f32_e32 v23, v23
	v_exp_f32_e32 v6, v6
	v_exp_f32_e32 v7, v7
	v_exp_f32_e32 v24, v24
	v_exp_f32_e32 v25, v25
	v_pk_add_f32 v[152:153], v[20:21], v[18:19]
	v_pk_add_f32 v[154:155], v[4:5], v[2:3]
	v_pk_add_f32 v[156:157], v[22:23], v[152:153]
	v_pk_add_f32 v[158:159], v[6:7], v[154:155]
	v_cvt_pk_f16_f32 v152, v18, v19
	v_cvt_pk_f16_f32 v153, v20, v21
	v_cvt_pk_f16_f32 v154, v22, v23
	v_cvt_pk_f16_f32 v155, v24, v25
	v_exp_f32_e32 v26, v26
	v_exp_f32_e32 v27, v27
	s_waitcnt lgkmcnt(0)
	v_mfma_f32_32x32x16_f16 v[50:65], v[126:129], v[152:155], v[50:65]
	v_exp_f32_e32 v28, v28
	v_exp_f32_e32 v29, v29
	v_exp_f32_e32 v30, v30
	v_exp_f32_e32 v31, v31
	v_exp_f32_e32 v32, v32
	v_exp_f32_e32 v33, v33
	v_exp_f32_e32 v8, v8
	v_mfma_f32_32x32x16_f16 v[34:49], v[122:125], v[152:155], v[34:49]
	v_cvt_pk_f16_f32 v122, v26, v27
	v_cvt_pk_f16_f32 v123, v28, v29
	v_cvt_pk_f16_f32 v124, v30, v31
	v_cvt_pk_f16_f32 v125, v32, v33
	v_exp_f32_e32 v9, v9
	ds_read_b64_tr_b16 v[126:127], v149 offset:12288
	ds_read_b64_tr_b16 v[128:129], v150 offset:12288
	v_exp_f32_e32 v10, v10
	v_mfma_f32_32x32x16_f16 v[50:65], v[118:121], v[122:125], v[50:65]
	v_exp_f32_e32 v11, v11
	v_exp_f32_e32 v12, v12
	v_exp_f32_e32 v13, v13
	v_cvt_pk_f16_f32 v118, v2, v3
	v_cvt_pk_f16_f32 v119, v4, v5
	v_cvt_pk_f16_f32 v120, v6, v7
	v_cvt_pk_f16_f32 v121, v8, v9
	v_mfma_f32_32x32x16_f16 v[34:49], v[114:117], v[122:125], v[34:49]
	ds_read_b64_tr_b16 v[114:115], v147 offset:12288
	ds_read_b64_tr_b16 v[116:117], v148 offset:12288
	ds_read_b64_tr_b16 v[122:123], v149 offset:14336
	ds_read_b64_tr_b16 v[124:125], v150 offset:14336
	v_add_f32_e64 v156, v24, v156
	v_add_f32_e64 v157, v25, v157
	v_pk_add_f32 v[158:159], v[8:9], v[158:159]
	v_exp_f32_e32 v14, v14
	v_exp_f32_e32 v15, v15
	v_exp_f32_e32 v16, v16
	v_exp_f32_e32 v17, v17
	s_waitcnt lgkmcnt(4)
	v_mfma_f32_32x32x16_f16 v[50:65], v[126:129], v[118:121], v[50:65]
	v_add_f32_e64 v126, v26, v156
	v_add_f32_e64 v127, v27, v157
	v_add_f32_e64 v128, v10, v158
	v_add_f32_e64 v129, v11, v159
	v_add_f32_e64 v152, v28, v126
	v_add_f32_e64 v153, v29, v127
	v_pk_add_f32 v[154:155], v[12:13], v[128:129]
	ds_read_b64_tr_b16 v[126:127], v147 offset:14336
	ds_read_b64_tr_b16 v[128:129], v148 offset:14336
	s_and_b64 vcc, exec, s[34:35]
	s_waitcnt lgkmcnt(4)
	v_mfma_f32_32x32x16_f16 v[34:49], v[114:117], v[118:121], v[34:49]
	v_cvt_pk_f16_f32 v114, v10, v11
	v_cvt_pk_f16_f32 v115, v12, v13
	v_cvt_pk_f16_f32 v116, v14, v15
	v_cvt_pk_f16_f32 v117, v16, v17
	v_add_f32_e64 v118, v30, v152
	v_add_f32_e64 v119, v31, v153
	v_pk_add_f32 v[120:121], v[14:15], v[154:155]
	v_pk_add_f32 v[118:119], v[32:33], v[118:119]
	s_waitcnt lgkmcnt(2)
	v_mfma_f32_32x32x16_f16 v[50:65], v[122:125], v[114:117], v[50:65]
	v_add_f32_e64 v120, v16, v120
	v_add_f32_e64 v121, v17, v121
	v_add_f32_e64 v118, v120, v118
	v_add_f32_e64 v119, v121, v119
	v_add_f32_e32 v118, v118, v119
	v_add_f32_e32 v145, v145, v118
	s_waitcnt lgkmcnt(0)
	v_mfma_f32_32x32x16_f16 v[34:49], v[126:129], v[114:117], v[34:49]
	v_mov_b32_e32 v114, 0
	s_cbranch_vccnz .LBB0_982
	s_mov_b32 s28, 0x41000000
	v_cmp_lg_f32_e64 s[34:35], s1, v151
	v_cmp_lt_f32_e32 vcc, s28, v151
	s_and_b64 s[30:31], s[30:31], s[34:35]
	s_or_b64 s[30:31], vcc, s[30:31]
	v_cndmask_b32_e64 v114, 0, 1, s[30:31]
	v_cmp_ne_u32_e32 vcc, 0, v114
	s_cbranch_vccz .LBB0_981
	v_add_f32_e32 v114, v146, v151
	v_max_f32_e32 v115, v138, v138
	v_max_f32_e32 v138, v115, v114
	v_cmp_neq_f32_e32 vcc, s1, v138
	s_nop 1
	v_cndmask_b32_e32 v114, 0, v138, vcc
	v_sub_f32_e32 v114, v114, v146
	v_exp_f32_e64 v116, -v114
	s_nop 0
	v_pk_mul_f32 v[64:65], v[116:117], v[64:65] op_sel_hi:[0,1]
	v_pk_mul_f32 v[62:63], v[116:117], v[62:63] op_sel_hi:[0,1]
	v_pk_mul_f32 v[60:61], v[116:117], v[60:61] op_sel_hi:[0,1]
	v_pk_mul_f32 v[58:59], v[116:117], v[58:59] op_sel_hi:[0,1]
	v_pk_mul_f32 v[56:57], v[116:117], v[56:57] op_sel_hi:[0,1]
	v_pk_mul_f32 v[54:55], v[116:117], v[54:55] op_sel_hi:[0,1]
	v_pk_mul_f32 v[52:53], v[116:117], v[52:53] op_sel_hi:[0,1]
	v_pk_mul_f32 v[50:51], v[116:117], v[50:51] op_sel_hi:[0,1]
	v_pk_mul_f32 v[48:49], v[116:117], v[48:49] op_sel_hi:[0,1]
	v_pk_mul_f32 v[46:47], v[116:117], v[46:47] op_sel_hi:[0,1]
	v_pk_mul_f32 v[44:45], v[116:117], v[44:45] op_sel_hi:[0,1]
	v_pk_mul_f32 v[42:43], v[116:117], v[42:43] op_sel_hi:[0,1]
	v_pk_mul_f32 v[40:41], v[116:117], v[40:41] op_sel_hi:[0,1]
	v_pk_mul_f32 v[38:39], v[116:117], v[38:39] op_sel_hi:[0,1]
	v_pk_mul_f32 v[36:37], v[116:117], v[36:37] op_sel_hi:[0,1]
	v_pk_mul_f32 v[34:35], v[116:117], v[34:35] op_sel_hi:[0,1]
	v_mul_f32_e32 v145, v145, v116
	s_branch .LBB0_982

.LBB0_993:
	v_mov_b32_e32 v2, 0xff800000
	s_and_saveexec_b64 s[42:43], s[34:35]
	v_xor_b32_e32 v2, 0x80000000, v146
	s_or_b64 exec, exec, s[42:43]
	s_lshl_b32 s34, s44, 14
	v_add_u32_e32 v115, s34, v134
	ds_read_b128 v[116:119], v115
	v_mov_b32_e32 v3, v2
	v_mov_b64_e32 v[4:5], v[2:3]
	v_mov_b64_e32 v[6:7], v[2:3]
	v_mov_b64_e32 v[8:9], v[2:3]
	v_mov_b64_e32 v[10:11], v[2:3]
	v_mov_b64_e32 v[12:13], v[2:3]
	v_mov_b64_e32 v[14:15], v[2:3]
	v_mov_b64_e32 v[16:17], v[2:3]
	ds_read_b128 v[120:123], v115 offset:4096
	v_add_u32_e32 v115, s34, v135
	ds_read_b128 v[124:127], v115
	ds_read_b128 v[148:151], v115 offset:4096
	v_add_u32_e32 v115, s34, v136
	ds_read_b128 v[152:155], v115
	ds_read_b128 v[156:159], v115 offset:4096
	v_add_u32_e32 v115, s34, v137
	ds_read_b128 v[164:167], v115
	ds_read_b128 v[168:171], v115 offset:4096
	s_waitcnt lgkmcnt(7)
	s_nop 0
	v_mfma_f32_32x32x16_f16 v[18:33], v[116:119], v[98:101], v[2:17]
	s_waitcnt lgkmcnt(6)
	v_mfma_f32_32x32x16_f16 v[2:17], v[120:123], v[98:101], v[2:17]
	s_waitcnt lgkmcnt(5)
	v_mfma_f32_32x32x16_f16 v[18:33], v[124:127], v[102:105], v[18:33]
	s_waitcnt lgkmcnt(4)
	v_mfma_f32_32x32x16_f16 v[2:17], v[148:151], v[102:105], v[2:17]
	s_waitcnt lgkmcnt(3)
	v_mfma_f32_32x32x16_f16 v[18:33], v[152:155], v[106:109], v[18:33]
	s_waitcnt lgkmcnt(2)
	v_mfma_f32_32x32x16_f16 v[2:17], v[156:159], v[106:109], v[2:17]
	s_waitcnt lgkmcnt(1)
	v_mfma_f32_32x32x16_f16 v[18:33], v[164:167], v[110:113], v[18:33]
	s_waitcnt lgkmcnt(0)
	v_mfma_f32_32x32x16_f16 v[2:17], v[168:171], v[110:113], v[2:17]

.LBB0_1002:
	v_exp_f32_e32 v82, v82
	v_exp_f32_e32 v83, v83
	v_exp_f32_e32 v66, v66
	v_exp_f32_e32 v67, v67
	v_exp_f32_e32 v84, v84
	v_exp_f32_e32 v85, v85
	v_exp_f32_e32 v68, v68
	v_exp_f32_e32 v69, v69
	v_exp_f32_e32 v86, v86
	v_exp_f32_e32 v87, v87
	v_exp_f32_e32 v70, v70
	v_exp_f32_e32 v71, v71
	v_exp_f32_e32 v88, v88
	v_exp_f32_e32 v89, v89
	v_pk_add_f32 v[152:153], v[84:85], v[82:83]
	v_pk_add_f32 v[154:155], v[68:69], v[66:67]
	v_pk_add_f32 v[156:157], v[86:87], v[152:153]
	v_pk_add_f32 v[158:159], v[70:71], v[154:155]
	v_cvt_pk_f16_f32 v152, v82, v83
	v_cvt_pk_f16_f32 v153, v84, v85
	v_cvt_pk_f16_f32 v154, v86, v87
	v_cvt_pk_f16_f32 v155, v88, v89
	v_exp_f32_e32 v90, v90
	v_exp_f32_e32 v91, v91
	s_waitcnt lgkmcnt(0)
	v_mfma_f32_32x32x16_f16 v[50:65], v[126:129], v[152:155], v[50:65]
	v_exp_f32_e32 v92, v92
	v_exp_f32_e32 v93, v93
	v_exp_f32_e32 v94, v94
	v_exp_f32_e32 v95, v95
	v_exp_f32_e32 v96, v96
	v_exp_f32_e32 v97, v97
	v_exp_f32_e32 v72, v72
	v_mfma_f32_32x32x16_f16 v[34:49], v[122:125], v[152:155], v[34:49]
	v_cvt_pk_f16_f32 v122, v90, v91
	v_cvt_pk_f16_f32 v123, v92, v93
	v_cvt_pk_f16_f32 v124, v94, v95
	v_cvt_pk_f16_f32 v125, v96, v97
	v_exp_f32_e32 v73, v73
	ds_read_b64_tr_b16 v[126:127], v149 offset:12288
	ds_read_b64_tr_b16 v[128:129], v150 offset:12288
	v_exp_f32_e32 v74, v74
	v_mfma_f32_32x32x16_f16 v[50:65], v[118:121], v[122:125], v[50:65]
	v_exp_f32_e32 v75, v75
	v_exp_f32_e32 v76, v76
	v_exp_f32_e32 v77, v77
	v_cvt_pk_f16_f32 v118, v66, v67
	v_cvt_pk_f16_f32 v119, v68, v69
	v_cvt_pk_f16_f32 v120, v70, v71
	v_cvt_pk_f16_f32 v121, v72, v73
	v_mfma_f32_32x32x16_f16 v[34:49], v[114:117], v[122:125], v[34:49]
	ds_read_b64_tr_b16 v[114:115], v147 offset:12288
	ds_read_b64_tr_b16 v[116:117], v148 offset:12288
	ds_read_b64_tr_b16 v[122:123], v149 offset:14336
	ds_read_b64_tr_b16 v[124:125], v150 offset:14336
	v_add_f32_e64 v156, v88, v156
	v_add_f32_e64 v157, v89, v157
	v_pk_add_f32 v[158:159], v[72:73], v[158:159]
	v_exp_f32_e32 v78, v78
	v_exp_f32_e32 v79, v79
	v_exp_f32_e32 v80, v80
	v_exp_f32_e32 v81, v81
	s_waitcnt lgkmcnt(4)
	v_mfma_f32_32x32x16_f16 v[50:65], v[126:129], v[118:121], v[50:65]
	v_add_f32_e64 v126, v90, v156
	v_add_f32_e64 v127, v91, v157
	v_add_f32_e64 v128, v74, v158
	v_add_f32_e64 v129, v75, v159
	v_add_f32_e64 v152, v92, v126
	v_add_f32_e64 v153, v93, v127
	v_pk_add_f32 v[154:155], v[76:77], v[128:129]
	ds_read_b64_tr_b16 v[126:127], v147 offset:14336
	ds_read_b64_tr_b16 v[128:129], v148 offset:14336
	s_and_b64 vcc, exec, s[34:35]
	s_waitcnt lgkmcnt(4)
	v_mfma_f32_32x32x16_f16 v[34:49], v[114:117], v[118:121], v[34:49]
	v_cvt_pk_f16_f32 v114, v74, v75
	v_cvt_pk_f16_f32 v115, v76, v77
	v_cvt_pk_f16_f32 v116, v78, v79
	v_cvt_pk_f16_f32 v117, v80, v81
	v_add_f32_e64 v118, v94, v152
	v_add_f32_e64 v119, v95, v153
	v_pk_add_f32 v[120:121], v[78:79], v[154:155]
	v_pk_add_f32 v[118:119], v[96:97], v[118:119]
	s_waitcnt lgkmcnt(2)
	v_mfma_f32_32x32x16_f16 v[50:65], v[122:125], v[114:117], v[50:65]
	v_add_f32_e64 v120, v80, v120
	v_add_f32_e64 v121, v81, v121
	v_add_f32_e64 v118, v118, v120
	v_add_f32_e64 v119, v119, v121
	v_add_f32_e32 v118, v118, v119
	v_add_f32_e32 v145, v145, v118
	s_waitcnt lgkmcnt(0)
	v_mfma_f32_32x32x16_f16 v[34:49], v[126:129], v[114:117], v[34:49]
	v_mov_b32_e32 v114, 0
	s_cbranch_vccnz .LBB0_1007
	s_mov_b32 s28, 0x41000000
	v_cmp_lg_f32_e64 s[34:35], s1, v151
	v_cmp_lt_f32_e32 vcc, s28, v151
	s_and_b64 s[30:31], s[30:31], s[34:35]
	s_or_b64 s[30:31], vcc, s[30:31]
	v_cndmask_b32_e64 v114, 0, 1, s[30:31]
	v_cmp_ne_u32_e32 vcc, 0, v114
	s_cbranch_vccz .LBB0_1006
	v_add_f32_e32 v114, v146, v151
	v_max_f32_e32 v115, v138, v138
	v_max_f32_e32 v138, v115, v114
	v_cmp_neq_f32_e32 vcc, s1, v138
	s_nop 1
	v_cndmask_b32_e32 v114, 0, v138, vcc
	v_sub_f32_e32 v114, v114, v146
	v_exp_f32_e64 v116, -v114
	s_nop 0
	v_pk_mul_f32 v[64:65], v[116:117], v[64:65] op_sel_hi:[0,1]
	v_pk_mul_f32 v[62:63], v[116:117], v[62:63] op_sel_hi:[0,1]
	v_pk_mul_f32 v[60:61], v[116:117], v[60:61] op_sel_hi:[0,1]
	v_pk_mul_f32 v[58:59], v[116:117], v[58:59] op_sel_hi:[0,1]
	v_pk_mul_f32 v[56:57], v[116:117], v[56:57] op_sel_hi:[0,1]
	v_pk_mul_f32 v[54:55], v[116:117], v[54:55] op_sel_hi:[0,1]
	v_pk_mul_f32 v[52:53], v[116:117], v[52:53] op_sel_hi:[0,1]
	v_pk_mul_f32 v[50:51], v[116:117], v[50:51] op_sel_hi:[0,1]
	v_pk_mul_f32 v[48:49], v[116:117], v[48:49] op_sel_hi:[0,1]
	v_pk_mul_f32 v[46:47], v[116:117], v[46:47] op_sel_hi:[0,1]
	v_pk_mul_f32 v[44:45], v[116:117], v[44:45] op_sel_hi:[0,1]
	v_pk_mul_f32 v[42:43], v[116:117], v[42:43] op_sel_hi:[0,1]
	v_pk_mul_f32 v[40:41], v[116:117], v[40:41] op_sel_hi:[0,1]
	v_pk_mul_f32 v[38:39], v[116:117], v[38:39] op_sel_hi:[0,1]
	v_pk_mul_f32 v[36:37], v[116:117], v[36:37] op_sel_hi:[0,1]
	v_pk_mul_f32 v[34:35], v[116:117], v[34:35] op_sel_hi:[0,1]
	v_mul_f32_e32 v145, v145, v116
	s_branch .LBB0_1007

; #define FA_PVD(src_, ks_) do { _Pragma("unroll") for (int blk = 0; blk < NB_; ++blk) o[blk] = __builtin_amdgcn_mfma_f32_32x32x16_f16(src_[blk], pf[ks_], o[blk], 0, 0, 0); } while (0)
; template <int DQK, int DV, int MODE, int S> ...
;     ...
;             const float mu = (m == -INFINITY) ? 0.f : m;
;             f32x2 lsa = {0.f, 0.f}, lsb = {0.f, 0.f}; const f32x2 mu2v = {mu, mu};
; #pragma unroll
;             for (int r = 0; r < 16; r += 2) { const f32x2 d0 = (f32x2){p0[r], p0[r + 1]} - mu2v, d1 = (f32x2){p1[r], p1[r + 1]} - mu2v;
;                 p0[r] = __builtin_amdgcn_exp2f(d0.x); p0[r + 1] = __builtin_amdgcn_exp2f(d0.y); p1[r] = __builtin_amdgcn_exp2f(d1.x); p1[r + 1] = __builtin_amdgcn_exp2f(d1.y);
;                 lsa += (f32x2){p0[r], p0[r + 1]}; lsb += (f32x2){p1[r], p1[r + 1]}; }
;             lsa += lsb; l += lsa.x + lsa.y;
;             f16x8 pf[4]; pf[0] = pack8(p0, 0); pf[1] = pack8(p0, 8); pf[2] = pack8(p1, 0); pf[3] = pack8(p1, 8);
;             __builtin_amdgcn_sched_barrier(0);
;             FA_VREADD(vfb, 1); FA_PVD(vfa, 0); __builtin_amdgcn_sched_barrier(0);
;             FA_VREADD(vfa, 2); FA_PVD(vfb, 1); __builtin_amdgcn_sched_barrier(0);
;             FA_VREADD(vfb, 3); FA_PVD(vfa, 2); __builtin_amdgcn_sched_barrier(0);
;             FA_PVD(vfb, 3);
.LBB0_1034:
	v_cmp_neq_f32_e32 vcc, s1, v178
	s_nop 1
	v_cndmask_b32_e32 v186, 0, v178, vcc
	v_pk_add_f32 v[82:83], v[82:83], v[186:187] op_sel_hi:[1,0] neg_lo:[0,1] neg_hi:[0,1]
	v_pk_add_f32 v[66:67], v[66:67], v[186:187] op_sel_hi:[1,0] neg_lo:[0,1] neg_hi:[0,1]
	v_exp_f32_e32 v82, v82
	v_exp_f32_e32 v83, v83
	v_exp_f32_e32 v188, v66
	v_exp_f32_e32 v189, v67
	v_pk_add_f32 v[66:67], v[84:85], v[186:187] op_sel_hi:[1,0] neg_lo:[0,1] neg_hi:[0,1]
	v_pk_add_f32 v[68:69], v[68:69], v[186:187] op_sel_hi:[1,0] neg_lo:[0,1] neg_hi:[0,1]
	v_exp_f32_e32 v84, v66
	v_exp_f32_e32 v85, v67
	v_exp_f32_e32 v190, v68
	v_exp_f32_e32 v191, v69
	v_pk_add_f32 v[86:87], v[86:87], v[186:187] op_sel_hi:[1,0] neg_lo:[0,1] neg_hi:[0,1]
	v_pk_add_f32 v[70:71], v[70:71], v[186:187] op_sel_hi:[1,0] neg_lo:[0,1] neg_hi:[0,1]
	v_exp_f32_e32 v86, v86
	v_exp_f32_e32 v87, v87
	v_exp_f32_e32 v192, v70
	v_exp_f32_e32 v193, v71
	v_pk_add_f32 v[70:71], v[88:89], v[186:187] op_sel_hi:[1,0] neg_lo:[0,1] neg_hi:[0,1]
	v_pk_add_f32 v[72:73], v[72:73], v[186:187] op_sel_hi:[1,0] neg_lo:[0,1] neg_hi:[0,1]
	v_exp_f32_e32 v70, v70
	v_exp_f32_e32 v71, v71
	v_exp_f32_e32 v88, v72
	v_exp_f32_e32 v89, v73
	v_pk_add_f32 v[72:73], v[90:91], v[186:187] op_sel_hi:[1,0] neg_lo:[0,1] neg_hi:[0,1]
	v_pk_add_f32 v[74:75], v[74:75], v[186:187] op_sel_hi:[1,0] neg_lo:[0,1] neg_hi:[0,1]
	v_exp_f32_e32 v72, v72
	v_exp_f32_e32 v73, v73
	v_exp_f32_e32 v90, v74
	v_exp_f32_e32 v91, v75
	v_pk_add_f32 v[74:75], v[92:93], v[186:187] op_sel_hi:[1,0] neg_lo:[0,1] neg_hi:[0,1]
	v_pk_add_f32 v[76:77], v[76:77], v[186:187] op_sel_hi:[1,0] neg_lo:[0,1] neg_hi:[0,1]
	v_pk_add_f32 v[66:67], v[84:85], v[82:83]
	v_pk_add_f32 v[68:69], v[190:191], v[188:189]
	v_exp_f32_e32 v74, v74
	v_exp_f32_e32 v75, v75
	v_exp_f32_e32 v92, v76
	v_exp_f32_e32 v93, v77
	v_pk_add_f32 v[76:77], v[94:95], v[186:187] op_sel_hi:[1,0] neg_lo:[0,1] neg_hi:[0,1]
	v_pk_add_f32 v[78:79], v[78:79], v[186:187] op_sel_hi:[1,0] neg_lo:[0,1] neg_hi:[0,1]
	v_pk_add_f32 v[66:67], v[86:87], v[66:67]
	v_pk_add_f32 v[68:69], v[192:193], v[68:69]
	v_exp_f32_e32 v76, v76
	v_exp_f32_e32 v77, v77
	v_exp_f32_e32 v94, v78
	v_exp_f32_e32 v95, v79
	v_pk_add_f32 v[78:79], v[96:97], v[186:187] op_sel_hi:[1,0] neg_lo:[0,1] neg_hi:[0,1]
	v_pk_add_f32 v[80:81], v[80:81], v[186:187] op_sel_hi:[1,0] neg_lo:[0,1] neg_hi:[0,1]
	v_pk_add_f32 v[66:67], v[70:71], v[66:67]
	v_pk_add_f32 v[68:69], v[88:89], v[68:69]
	v_exp_f32_e32 v78, v78
	v_exp_f32_e32 v79, v79
	v_exp_f32_e32 v96, v80
	v_exp_f32_e32 v97, v81
	v_pk_add_f32 v[66:67], v[72:73], v[66:67]
	v_pk_add_f32 v[68:69], v[90:91], v[68:69]
	v_pk_add_f32 v[66:67], v[74:75], v[66:67]
	v_pk_add_f32 v[68:69], v[92:93], v[68:69]
	v_pk_add_f32 v[66:67], v[76:77], v[66:67]
	v_pk_add_f32 v[68:69], v[94:95], v[68:69]
	v_pk_add_f32 v[66:67], v[78:79], v[66:67]
	v_pk_add_f32 v[68:69], v[96:97], v[68:69]
	v_cvt_pk_f16_f32 v80, v94, v95
	v_pk_add_f32 v[66:67], v[68:69], v[66:67]
	v_cvt_pk_f16_f32 v68, v86, v87
	v_add_f32_e32 v186, v66, v67
	v_cvt_pk_f16_f32 v66, v82, v83
	v_cvt_pk_f16_f32 v67, v84, v85
	v_cvt_pk_f16_f32 v69, v70, v71
	v_cvt_pk_f16_f32 v70, v72, v73
	v_cvt_pk_f16_f32 v71, v74, v75
	v_cvt_pk_f16_f32 v72, v76, v77
	v_cvt_pk_f16_f32 v73, v78, v79
	v_cvt_pk_f16_f32 v74, v188, v189
	v_cvt_pk_f16_f32 v75, v190, v191
	v_cvt_pk_f16_f32 v76, v192, v193
	v_cvt_pk_f16_f32 v77, v88, v89
	v_cvt_pk_f16_f32 v78, v90, v91
	v_cvt_pk_f16_f32 v79, v92, v93
	v_cvt_pk_f16_f32 v81, v96, v97
	ds_read_b64_tr_b16 v[82:83], v0 offset:4096
	ds_read_b64_tr_b16 v[84:85], v179 offset:4096
	ds_read_b64_tr_b16 v[86:87], v180 offset:4096
	ds_read_b64_tr_b16 v[88:89], v181 offset:4096
	ds_read_b64_tr_b16 v[90:91], v182 offset:4096
	ds_read_b64_tr_b16 v[92:93], v183 offset:4096
	ds_read_b64_tr_b16 v[94:95], v184 offset:4096
	ds_read_b64_tr_b16 v[96:97], v185 offset:4096
	s_waitcnt lgkmcnt(14)
	v_mfma_f32_32x32x16_f16 v[50:65], v[138:141], v[66:69], v[50:65]
	s_waitcnt lgkmcnt(12)
	v_mfma_f32_32x32x16_f16 v[34:49], v[134:137], v[66:69], v[34:49]
	s_waitcnt lgkmcnt(10)
	v_mfma_f32_32x32x16_f16 v[18:33], v[142:145], v[66:69], v[18:33]
	s_waitcnt lgkmcnt(8)
	v_mfma_f32_32x32x16_f16 v[2:17], v[130:133], v[66:69], v[2:17]
	s_waitcnt lgkmcnt(6)
	v_mfma_f32_32x32x16_f16 v[50:65], v[82:85], v[70:73], v[50:65]
	v_add_f32_e32 v147, v147, v186
	s_waitcnt lgkmcnt(4)
	v_mfma_f32_32x32x16_f16 v[34:49], v[86:89], v[70:73], v[34:49]
	s_waitcnt lgkmcnt(2)
	v_mfma_f32_32x32x16_f16 v[18:33], v[90:93], v[70:73], v[18:33]
	ds_read_b64_tr_b16 v[66:67], v0 offset:8192
	ds_read_b64_tr_b16 v[68:69], v179 offset:8192
	ds_read_b64_tr_b16 v[82:83], v180 offset:8192
	ds_read_b64_tr_b16 v[84:85], v181 offset:8192
	ds_read_b64_tr_b16 v[86:87], v182 offset:8192
	ds_read_b64_tr_b16 v[88:89], v183 offset:8192
	ds_read_b64_tr_b16 v[90:91], v184 offset:8192
	ds_read_b64_tr_b16 v[92:93], v185 offset:8192
	s_waitcnt lgkmcnt(8)
	v_mfma_f32_32x32x16_f16 v[2:17], v[94:97], v[70:73], v[2:17]
	s_waitcnt lgkmcnt(6)
	v_mfma_f32_32x32x16_f16 v[50:65], v[66:69], v[74:77], v[50:65]
	s_waitcnt lgkmcnt(4)
	v_mfma_f32_32x32x16_f16 v[34:49], v[82:85], v[74:77], v[34:49]
	s_waitcnt lgkmcnt(2)
	v_mfma_f32_32x32x16_f16 v[18:33], v[86:89], v[74:77], v[18:33]
	ds_read_b64_tr_b16 v[66:67], v0 offset:12288
	ds_read_b64_tr_b16 v[68:69], v179 offset:12288
	ds_read_b64_tr_b16 v[70:71], v180 offset:12288
	ds_read_b64_tr_b16 v[72:73], v181 offset:12288
	ds_read_b64_tr_b16 v[82:83], v182 offset:12288
	ds_read_b64_tr_b16 v[84:85], v183 offset:12288
	ds_read_b64_tr_b16 v[86:87], v184 offset:12288
	ds_read_b64_tr_b16 v[88:89], v185 offset:12288
	s_waitcnt lgkmcnt(8)
	v_mfma_f32_32x32x16_f16 v[2:17], v[90:93], v[74:77], v[2:17]
	s_waitcnt lgkmcnt(6)
	v_mfma_f32_32x32x16_f16 v[50:65], v[66:69], v[78:81], v[50:65]
	s_waitcnt lgkmcnt(4)
	v_mfma_f32_32x32x16_f16 v[34:49], v[70:73], v[78:81], v[34:49]
	s_waitcnt lgkmcnt(2)
	v_mfma_f32_32x32x16_f16 v[18:33], v[82:85], v[78:81], v[18:33]
	s_waitcnt lgkmcnt(0)
	v_mfma_f32_32x32x16_f16 v[2:17], v[86:89], v[78:81], v[2:17]
